# conversion loops: f32 weight loads carry sc1 nt so the one-pass stream does not displace the GEMM panels
# baseline (speedup 1.0000x reference)
; __device__ __forceinline__ void ttb_load(TReg& R, const float* src, int ld, int k0, int n0, int tid) {
;     const int kr = tid >> 4, nq = tid & 15;
; #pragma unroll
;     for (int rep = 0; rep < 4; ++rep) R.v[rep] = __builtin_nontemporal_load((const f32x4*)(src + (size_t)(k0 + 4 * kr + rep) * ld + n0 + 4 * nq)); }
; __device__ __forceinline__ void ttb_put(const TReg& R, LAS unsigned* tile, int tid) {
;     const int kr = tid >> 4, nq = tid & 15;
; #pragma unroll
;     for (int c = 0; c < 4; ++c) { const int n = 4 * nq + c;
;         tile[n * 32 + (kr ^ (n & 31))] = pk4_fp8(R.v[0][c] * W_FP8_SCALE, R.v[1][c] * W_FP8_SCALE, R.v[2][c] * W_FP8_SCALE, R.v[3][c] * W_FP8_SCALE); } }
; __device__ __forceinline__ void ttb_finish(LAS const unsigned* tile, unsigned char* dst, int ldd, int k0, int n0, int map, int tid) {
;     const int n = tid >> 3, kq = tid & 7, m = n & 31, ns = n0 + n; int r = ns;
;     if (map == 2) { const int j = ns >> 1, par = ns & 1; r = 256 * (j >> 7) + 128 * par + (j & 127); }
;     const u32x4 g = *(LAS const u32x4*)(tile + n * 32 + 4 * (kq ^ (m >> 2)));
;     const unsigned a0 = (m & 1) ? g.y : g.x, a1 = (m & 1) ? g.x : g.y, a2 = (m & 1) ? g.w : g.z, a3 = (m & 1) ? g.z : g.w;
;     u32x4 w; w.x = (m & 2) ? a2 : a0; w.y = (m & 2) ? a3 : a1; w.z = (m & 2) ? a0 : a2; w.w = (m & 2) ? a1 : a3;
;     __builtin_nontemporal_store(w, (u32x4*)(dst + (size_t)r * ldd + k0 + 16 * kq));
; }
; template <int K_, int N_, int MAP_> __device__ __forceinline__ void tjob_b(const Ctx& C, int bid, int G, const float* src, unsigned char* dstb, int nbatch) {
; __global__ void __launch_bounds__(512, 2) mk_fwd(Args args) {
;     ...
;     if (IN(1)) for (int rep_ = 0; rep_ < 1 + ((MK_REPEAT >> 1) & 1); ++rep_) { if (rep_) xcd_barrier(bar);
;         const int nconv = (C.G % 8 == 0 && C.G >= 64) ? ((C.G * NCONV_16THS / 16) & ~7) : 0, Gg = C.G - nconv;
;         if (nconv == 0 || C.bid >= Gg) { const int cb = nconv ? C.bid - Gg : C.bid, cg = nconv ? nconv : C.G;
;     ...
;             for (int r2 = 0; r2 < MK_CONV2; ++r2) { tjob_b<2048, 4096, 2>(C, cb, cg, C.ka->in[I_WE1], C.ws + WS_W1T, NEXP); tjob_b<2048, 2048, 0>(C, cb, cg, C.ka->in[I_WE2], C.ws + WS_W2T, NEXP); }
;     ...
;             tjob_b<2048, 4096, 2>(C, cb, cg, C.ka->in[I_WE1], C.ws + WS_W1T, NEXP); tjob_b<2048, 2048, 0>(C, cb, cg, C.ka->in[I_WE2], C.ws + WS_W2T, nconv ? NEXP - E2_TAIL : NEXP); }
.LBB0_175:
	s_cmp_lt_i32 s72, 2
	s_cselect_b64 s[0:1], -1, 0
	s_cmp_gt_i32 s73, 1
	s_cselect_b64 s[2:3], -1, 0
	v_writelane_b32 v254, s60, 8
	s_and_b64 s[0:1], s[0:1], s[2:3]
	v_mov_b32_e32 v68, v0
	v_writelane_b32 v254, s61, 9
	v_cndmask_b32_e64 v1, 0, 1, s[0:1]
	v_writelane_b32 v254, s62, 10
	v_cmp_ne_u32_e64 s[4:5], 1, v1
	s_andn2_b64 vcc, exec, s[0:1]
	s_mov_b64 s[70:71], s[34:35]
	v_writelane_b32 v254, s63, 11
	s_cbranch_vccnz .LBB0_297
	v_readlane_b32 s0, v254, 2
	s_mov_b32 s6, s0
	s_and_b32 s0, s0, 7
	v_readlane_b32 s1, v254, 3
	s_cmp_eq_u32 s0, 0
	s_cselect_b64 s[0:1], -1, 0
	s_cmp_gt_i32 s6, 63
	s_cselect_b64 s[2:3], -1, 0
	s_mul_i32 s29, s6, 6
	s_and_b64 s[0:1], s[2:3], s[0:1]
	s_lshr_b32 s2, s29, 4
	s_and_b32 s2, s2, 0x7fffff8
	s_and_b64 s[0:1], s[0:1], exec
	s_cselect_b32 s30, s2, 0
	s_sub_i32 s28, s6, s30
	s_cmp_eq_u32 s30, 0
	s_cselect_b64 s[2:3], -1, 0
	s_cmp_lg_u32 s30, 0
	v_readlane_b32 s0, v254, 0
	s_cselect_b64 s[20:21], -1, 0
	s_cmp_lt_i32 s0, s28
	v_readlane_b32 s1, v254, 1
	s_cselect_b64 s[10:11], -1, 0
	s_and_b64 s[0:1], s[20:21], s[10:11]
	s_and_b64 vcc, exec, s[0:1]
	s_cbranch_vccnz .LBB0_228
	v_mov_b64_e32 v[2:3], s[70:71]
	flat_load_dwordx2 v[66:67], v[2:3] offset:184
	s_and_b64 s[0:1], s[2:3], exec
	s_cselect_b32 s0, 0, s28
	v_readlane_b32 s6, v254, 0
	s_sub_i32 s1, s6, s0
	v_readlane_b32 s7, v254, 1
	s_cmp_lt_i32 s1, 0x8000
	s_cselect_b64 s[6:7], -1, 0
	s_cmpk_gt_i32 s1, 0x7fff
	v_ashrrev_i32_e32 v69, 2, v68
	v_lshlrev_b32_e32 v74, 4, v68
	s_cbranch_scc1 .LBB0_179
	s_ashr_i32 s0, s1, 31
	s_lshr_b32 s0, s0, 22
	s_add_i32 s0, s1, s0
	s_ashr_i32 s8, s0, 10
	s_and_b32 s0, s0, 0xfc00
	s_sub_i32 s0, s1, s0
	s_sext_i32_i16 s12, s0
	s_bfe_u32 s12, s12, 0x4001b
	s_add_i32 s12, s0, s12
	s_sext_i32_i16 s13, s12
	s_and_b32 s12, s12, 0xfff0
	s_ashr_i32 s9, s8, 31
	s_sub_i32 s0, s0, s12
	s_lshl_b32 s12, s13, 2
	s_lshl_b64 s[8:9], s[8:9], 25
	s_sext_i32_i16 s0, s0
	s_andn2_b32 s12, s12, 63
	v_and_b32_e32 v1, -4, v69
	s_ashr_i32 s13, s12, 31
	s_waitcnt vmcnt(0) lgkmcnt(0)
	v_lshl_add_u64 v[2:3], v[66:67], 0, s[8:9]
	v_lshl_add_u32 v10, s0, 7, v1
	v_lshl_add_u64 v[2:3], s[12:13], 2, v[2:3]
	v_and_b32_e32 v4, 0xf0, v74
	v_mov_b32_e32 v5, 0
	v_ashrrev_i32_e32 v11, 31, v10
	v_lshl_add_u64 v[12:13], v[2:3], 0, v[4:5]
	v_lshlrev_b64 v[2:3], 14, v[10:11]
	v_lshl_add_u64 v[14:15], v[12:13], 0, v[2:3]
	v_or_b32_e32 v2, 1, v10
	v_ashrrev_i32_e32 v3, 31, v2
	v_lshlrev_b64 v[2:3], 14, v[2:3]
	v_lshl_add_u64 v[16:17], v[12:13], 0, v[2:3]
	global_load_dwordx4 v[2:5], v[14:15], off sc1 nt
	global_load_dwordx4 v[6:9], v[16:17], off sc1 nt
	v_or_b32_e32 v14, 2, v10
	v_ashrrev_i32_e32 v15, 31, v14
	v_or_b32_e32 v10, 3, v10
	v_lshlrev_b64 v[14:15], 14, v[14:15]
	v_ashrrev_i32_e32 v11, 31, v10
	v_lshl_add_u64 v[18:19], v[12:13], 0, v[14:15]
	v_lshlrev_b64 v[10:11], 14, v[10:11]
	v_lshl_add_u64 v[20:21], v[12:13], 0, v[10:11]
	global_load_dwordx4 v[10:13], v[18:19], off sc1 nt
	global_load_dwordx4 v[14:17], v[20:21], off sc1 nt
.LBB0_179:
	s_and_b64 s[8:9], s[2:3], exec
	v_readlane_b32 s8, v254, 2
	s_cselect_b32 s0, s8, s30
	s_add_i32 s22, s1, s0
	s_cmpk_gt_i32 s22, 0x7fff
	v_readlane_b32 s9, v254, 3
	s_cbranch_scc1 .LBB0_181
	s_ashr_i32 s8, s22, 31
	s_lshr_b32 s8, s8, 22
	s_add_i32 s9, s22, s8
	s_ashr_i32 s8, s9, 10
	s_and_b32 s9, s9, 0xfc00
	s_sub_i32 s12, s22, s9
	s_sext_i32_i16 s13, s12
	s_bfe_u32 s13, s13, 0x4001b
	s_add_i32 s13, s12, s13
	s_sext_i32_i16 s14, s13
	s_and_b32 s13, s13, 0xfff0
	s_sub_i32 s12, s12, s13
	s_ashr_i32 s9, s8, 31
	s_sext_i32_i16 s15, s12
	s_lshl_b32 s12, s14, 2
	s_lshl_b64 s[8:9], s[8:9], 25
	s_andn2_b32 s12, s12, 63
	v_and_b32_e32 v1, -4, v69
	s_ashr_i32 s13, s12, 31
	s_waitcnt vmcnt(0) lgkmcnt(0)
	v_lshl_add_u64 v[18:19], v[66:67], 0, s[8:9]
	v_lshl_add_u32 v26, s15, 7, v1
	v_lshl_add_u64 v[18:19], s[12:13], 2, v[18:19]
	v_and_b32_e32 v20, 0xf0, v74
	v_mov_b32_e32 v21, 0
	v_ashrrev_i32_e32 v27, 31, v26
	v_lshl_add_u64 v[28:29], v[18:19], 0, v[20:21]
	v_lshlrev_b64 v[18:19], 14, v[26:27]
	v_lshl_add_u64 v[30:31], v[28:29], 0, v[18:19]
	v_or_b32_e32 v18, 1, v26
	v_ashrrev_i32_e32 v19, 31, v18
	v_lshlrev_b64 v[18:19], 14, v[18:19]
	v_lshl_add_u64 v[32:33], v[28:29], 0, v[18:19]
	global_load_dwordx4 v[18:21], v[30:31], off sc1 nt
	global_load_dwordx4 v[22:25], v[32:33], off sc1 nt
	v_or_b32_e32 v30, 2, v26
	v_ashrrev_i32_e32 v31, 31, v30
	v_or_b32_e32 v26, 3, v26
	v_lshlrev_b64 v[30:31], 14, v[30:31]
	v_ashrrev_i32_e32 v27, 31, v26
	v_lshl_add_u64 v[34:35], v[28:29], 0, v[30:31]
	v_lshlrev_b64 v[26:27], 14, v[26:27]
	v_lshl_add_u64 v[36:37], v[28:29], 0, v[26:27]
	global_load_dwordx4 v[26:29], v[34:35], off sc1 nt
	global_load_dwordx4 v[30:33], v[36:37], off sc1 nt
; #define LAS __attribute__((address_space(3)))
; #define TB_LOAD(R_, t_) do { const int _t = (t_); if (_t < tot) { const int _b = _t / per, _r = _t % per; ttb_load(R_, src + (size_t)_b * K_ * N_, N_, (_r % kt) * 128, (_r / kt) * 64, C.tid); } } while (0)
; __device__ __forceinline__ void ttb_load(TReg& R, const float* src, int ld, int k0, int n0, int tid) {
;     const int kr = tid >> 4, nq = tid & 15;
; #pragma unroll
;     for (int rep = 0; rep < 4; ++rep) R.v[rep] = __builtin_nontemporal_load((const f32x4*)(src + (size_t)(k0 + 4 * kr + rep) * ld + n0 + 4 * nq)); }
; __device__ __forceinline__ void ttb_put(const TReg& R, LAS unsigned* tile, int tid) {
;     const int kr = tid >> 4, nq = tid & 15;
; #pragma unroll
;     for (int c = 0; c < 4; ++c) { const int n = 4 * nq + c;
;         tile[n * 32 + (kr ^ (n & 31))] = pk4_fp8(R.v[0][c] * W_FP8_SCALE, R.v[1][c] * W_FP8_SCALE, R.v[2][c] * W_FP8_SCALE, R.v[3][c] * W_FP8_SCALE); } }
; __device__ __forceinline__ void ttb_finish(LAS const unsigned* tile, unsigned char* dst, int ldd, int k0, int n0, int map, int tid) {
;     const int n = tid >> 3, kq = tid & 7, m = n & 31, ns = n0 + n; int r = ns;
;     if (map == 2) { const int j = ns >> 1, par = ns & 1; r = 256 * (j >> 7) + 128 * par + (j & 127); }
;     const u32x4 g = *(LAS const u32x4*)(tile + n * 32 + 4 * (kq ^ (m >> 2)));
;     const unsigned a0 = (m & 1) ? g.y : g.x, a1 = (m & 1) ? g.x : g.y, a2 = (m & 1) ? g.w : g.z, a3 = (m & 1) ? g.z : g.w;
;     u32x4 w; w.x = (m & 2) ? a2 : a0; w.y = (m & 2) ? a3 : a1; w.z = (m & 2) ? a0 : a2; w.w = (m & 2) ? a1 : a3;
;     __builtin_nontemporal_store(w, (u32x4*)(dst + (size_t)r * ldd + k0 + 16 * kq));
; }
; template <int K_, int N_, int MAP_> __device__ __forceinline__ void tjob_b(const Ctx& C, int bid, int G, const float* src, unsigned char* dstb, int nbatch) {
;     constexpr int kt = K_ / 128, ntile = N_ / 64, per = kt * ntile; const int tot = per * nbatch;
;     TReg R0, R1, R2, R3; int kbuf = 0;
;     ...
;     TB_LOAD(R0, bid); TB_LOAD(R1, bid + G); TB_LOAD(R2, bid + 2 * G); TB_LOAD(R3, bid + 3 * G);
.LBB0_181:
	s_add_i32 s23, s22, s0
	s_cmpk_gt_i32 s23, 0x7fff
	s_cbranch_scc1 .LBB0_183
	s_ashr_i32 s8, s23, 31
	s_lshr_b32 s8, s8, 22
	s_add_i32 s9, s23, s8
	s_ashr_i32 s8, s9, 10
	s_and_b32 s9, s9, 0xfc00
	s_sub_i32 s12, s23, s9
	s_sext_i32_i16 s13, s12
	s_bfe_u32 s13, s13, 0x4001b
	s_add_i32 s13, s12, s13
	s_sext_i32_i16 s14, s13
	s_and_b32 s13, s13, 0xfff0
	s_sub_i32 s12, s12, s13
	s_ashr_i32 s9, s8, 31
	s_sext_i32_i16 s15, s12
	s_lshl_b32 s12, s14, 2
	s_lshl_b64 s[8:9], s[8:9], 25
	s_andn2_b32 s12, s12, 63
	v_and_b32_e32 v1, -4, v69
	s_ashr_i32 s13, s12, 31
	s_waitcnt vmcnt(0) lgkmcnt(0)
	v_lshl_add_u64 v[34:35], v[66:67], 0, s[8:9]
	v_lshl_add_u32 v42, s15, 7, v1
	v_lshl_add_u64 v[34:35], s[12:13], 2, v[34:35]
	v_and_b32_e32 v36, 0xf0, v74
	v_mov_b32_e32 v37, 0
	v_ashrrev_i32_e32 v43, 31, v42
	v_lshl_add_u64 v[44:45], v[34:35], 0, v[36:37]
	v_lshlrev_b64 v[34:35], 14, v[42:43]
	v_lshl_add_u64 v[46:47], v[44:45], 0, v[34:35]
	v_or_b32_e32 v34, 1, v42
	v_ashrrev_i32_e32 v35, 31, v34
	v_lshlrev_b64 v[34:35], 14, v[34:35]
	v_lshl_add_u64 v[48:49], v[44:45], 0, v[34:35]
	global_load_dwordx4 v[34:37], v[46:47], off sc1 nt
	global_load_dwordx4 v[38:41], v[48:49], off sc1 nt
	v_or_b32_e32 v46, 2, v42
	v_ashrrev_i32_e32 v47, 31, v46
	v_or_b32_e32 v42, 3, v42
	v_lshlrev_b64 v[46:47], 14, v[46:47]
	v_ashrrev_i32_e32 v43, 31, v42
	v_lshl_add_u64 v[50:51], v[44:45], 0, v[46:47]
	v_lshlrev_b64 v[42:43], 14, v[42:43]
	v_lshl_add_u64 v[52:53], v[44:45], 0, v[42:43]
	global_load_dwordx4 v[42:45], v[50:51], off sc1 nt
	global_load_dwordx4 v[46:49], v[52:53], off sc1 nt
.LBB0_183:
	s_add_i32 s24, s23, s0
	s_cmpk_gt_i32 s24, 0x7fff
	s_cbranch_scc1 .LBB0_185
	s_ashr_i32 s8, s24, 31
	s_lshr_b32 s8, s8, 22
	s_add_i32 s9, s24, s8
	s_ashr_i32 s8, s9, 10
	s_and_b32 s9, s9, 0xfc00
	s_sub_i32 s12, s24, s9
	s_sext_i32_i16 s13, s12
	s_bfe_u32 s13, s13, 0x4001b
	s_add_i32 s13, s12, s13
	s_sext_i32_i16 s14, s13
	s_and_b32 s13, s13, 0xfff0
	s_sub_i32 s12, s12, s13
	s_ashr_i32 s9, s8, 31
	s_sext_i32_i16 s15, s12
	s_lshl_b32 s12, s14, 2
	s_lshl_b64 s[8:9], s[8:9], 25
	s_andn2_b32 s12, s12, 63
	v_and_b32_e32 v1, -4, v69
	s_ashr_i32 s13, s12, 31
	s_waitcnt vmcnt(0) lgkmcnt(0)
	v_lshl_add_u64 v[50:51], v[66:67], 0, s[8:9]
	v_lshl_add_u32 v58, s15, 7, v1
	v_lshl_add_u64 v[50:51], s[12:13], 2, v[50:51]
	v_and_b32_e32 v52, 0xf0, v74
	v_mov_b32_e32 v53, 0
	v_ashrrev_i32_e32 v59, 31, v58
	v_lshl_add_u64 v[60:61], v[50:51], 0, v[52:53]
	v_lshlrev_b64 v[50:51], 14, v[58:59]
	v_lshl_add_u64 v[62:63], v[60:61], 0, v[50:51]
	v_or_b32_e32 v50, 1, v58
	v_ashrrev_i32_e32 v51, 31, v50
	v_lshlrev_b64 v[50:51], 14, v[50:51]
	v_lshl_add_u64 v[64:65], v[60:61], 0, v[50:51]
	global_load_dwordx4 v[50:53], v[62:63], off sc1 nt
	global_load_dwordx4 v[54:57], v[64:65], off sc1 nt
	v_or_b32_e32 v62, 2, v58
	v_ashrrev_i32_e32 v63, 31, v62
	v_or_b32_e32 v58, 3, v58
	v_lshlrev_b64 v[62:63], 14, v[62:63]
	v_ashrrev_i32_e32 v59, 31, v58
	v_lshl_add_u64 v[70:71], v[60:61], 0, v[62:63]
	v_lshlrev_b64 v[58:59], 14, v[58:59]
	v_lshl_add_u64 v[72:73], v[60:61], 0, v[58:59]
	global_load_dwordx4 v[58:61], v[70:71], off sc1 nt
	global_load_dwordx4 v[62:65], v[72:73], off sc1 nt

; #define LAS __attribute__((address_space(3)))
; __device__ __forceinline__ void ttb_put(const TReg& R, LAS unsigned* tile, int tid) {
;     const int kr = tid >> 4, nq = tid & 15;
; #pragma unroll
;     for (int c = 0; c < 4; ++c) { const int n = 4 * nq + c;
;         tile[n * 32 + (kr ^ (n & 31))] = pk4_fp8(R.v[0][c] * W_FP8_SCALE, R.v[1][c] * W_FP8_SCALE, R.v[2][c] * W_FP8_SCALE, R.v[3][c] * W_FP8_SCALE); } }
.Lcv_j1_0:
	v_mul_f32_e32 v72, 0x43800000, v2
	v_mul_f32_e32 v93, 0x43800000, v6
	v_med3_f32 v72, v72, s31, v87
	v_med3_f32 v93, v93, s31, v87
	v_cvt_pk_fp8_f32 v95, v72, v93
	v_mul_f32_e32 v94, 0x43800000, v10
	v_mul_f32_e32 v72, 0x43800000, v14
	v_med3_f32 v93, v94, s31, v87
	v_med3_f32 v72, v72, s31, v87
	v_cvt_pk_fp8_f32 v95, v93, v72 op_sel:[0,0,1]
	v_mul_f32_e32 v72, 0x43800000, v3
	v_mul_f32_e32 v93, 0x43800000, v7
	v_med3_f32 v72, v72, s31, v87
	v_med3_f32 v93, v93, s31, v87
	v_cvt_pk_fp8_f32 v96, v72, v93
	v_mul_f32_e32 v94, 0x43800000, v11
	v_mul_f32_e32 v72, 0x43800000, v15
	v_med3_f32 v93, v94, s31, v87
	v_med3_f32 v72, v72, s31, v87
	s_lshl_b32 s12, s27, 13
	v_cvt_pk_fp8_f32 v96, v93, v72 op_sel:[0,0,1]
	s_add_i32 s35, s12, 0
	v_add3_u32 v72, s35, v80, v88
	ds_write_b32 v72, v95
	v_add3_u32 v72, s35, v81, v89
	ds_write_b32 v72, v96
	v_mul_f32_e32 v72, 0x43800000, v4
	v_mul_f32_e32 v93, 0x43800000, v8
	v_med3_f32 v72, v72, s31, v87
	v_med3_f32 v93, v93, s31, v87
	v_cvt_pk_fp8_f32 v95, v72, v93
	v_mul_f32_e32 v94, 0x43800000, v12
	v_mul_f32_e32 v72, 0x43800000, v16
	v_med3_f32 v93, v94, s31, v87
	v_med3_f32 v72, v72, s31, v87
	v_cvt_pk_fp8_f32 v95, v93, v72 op_sel:[0,0,1]
	v_mul_f32_e32 v72, 0x43800000, v5
	v_mul_f32_e32 v93, 0x43800000, v9
	v_med3_f32 v72, v72, s31, v87
	v_med3_f32 v93, v93, s31, v87
	v_cvt_pk_fp8_f32 v96, v72, v93
	v_mul_f32_e32 v94, 0x43800000, v13
	v_mul_f32_e32 v72, 0x43800000, v17
	v_med3_f32 v93, v94, s31, v87
	v_med3_f32 v72, v72, s31, v87
	v_cvt_pk_fp8_f32 v96, v93, v72 op_sel:[0,0,1]
	s_add_i32 s33, s34, s16
	s_cmpk_gt_i32 s33, 0x7fff
	v_add3_u32 v72, s35, v82, v90
	s_cselect_b64 s[12:13], -1, 0
	ds_write_b32 v72, v95
	v_add3_u32 v72, s35, v83, v91
	s_and_b64 vcc, exec, s[12:13]
	ds_write_b32 v72, v96
	s_cbranch_vccnz .LBB0_191
	s_ashr_i32 s36, s33, 31
	s_lshr_b32 s36, s36, 22
	s_add_i32 s37, s33, s36
	s_ashr_i32 s36, s37, 10
	s_and_b32 s37, s37, 0xfc00
	s_sub_i32 s38, s33, s37
	s_ashr_i32 s37, s36, 31
	s_lshl_b64 s[36:37], s[36:37], 25
	v_lshl_add_u64 v[2:3], v[66:67], 0, s[36:37]
	s_sext_i32_i16 s36, s38
	s_bfe_u32 s36, s36, 0x4001b
	s_add_i32 s36, s38, s36
	s_sext_i32_i16 s37, s36
	s_and_b32 s36, s36, 0xfff0
	s_sub_i32 s36, s38, s36
	s_sext_i32_i16 s38, s36
	s_lshl_b32 s36, s37, 2
	s_andn2_b32 s36, s36, 63
	v_lshl_add_u32 v10, s38, 7, v86
	s_ashr_i32 s37, s36, 31
	v_lshl_add_u64 v[2:3], s[36:37], 2, v[2:3]
	v_lshlrev_b32_e32 v72, 2, v68
	v_ashrrev_i32_e32 v11, 31, v10
	v_lshl_add_u64 v[12:13], v[2:3], 0, v[72:73]
	v_lshlrev_b64 v[2:3], 14, v[10:11]
	v_or_b32_e32 v4, 1, v10
	v_or_b32_e32 v14, 2, v10
	v_or_b32_e32 v10, 3, v10
	v_ashrrev_i32_e32 v5, 31, v4
	v_ashrrev_i32_e32 v15, 31, v14
	v_ashrrev_i32_e32 v11, 31, v10
	v_lshlrev_b64 v[4:5], 14, v[4:5]
	v_lshlrev_b64 v[14:15], 14, v[14:15]
	v_lshlrev_b64 v[10:11], 14, v[10:11]
	v_lshl_add_u64 v[2:3], v[12:13], 0, v[2:3]
	v_lshl_add_u64 v[6:7], v[12:13], 0, v[4:5]
	v_lshl_add_u64 v[14:15], v[12:13], 0, v[14:15]
	v_lshl_add_u64 v[16:17], v[12:13], 0, v[10:11]
	global_load_dwordx4 v[2:5], v[2:3], off sc1 nt
	s_nop 0
	global_load_dwordx4 v[6:9], v[6:7], off sc1 nt
	s_nop 0
	global_load_dwordx4 v[10:13], v[14:15], off sc1 nt
	s_nop 0
	global_load_dwordx4 v[14:17], v[16:17], off sc1 nt

; #define LAS __attribute__((address_space(3)))
; __device__ __forceinline__ void ttb_put(const TReg& R, LAS unsigned* tile, int tid) {
;     const int kr = tid >> 4, nq = tid & 15;
; #pragma unroll
;     for (int c = 0; c < 4; ++c) { const int n = 4 * nq + c;
;         tile[n * 32 + (kr ^ (n & 31))] = pk4_fp8(R.v[0][c] * W_FP8_SCALE, R.v[1][c] * W_FP8_SCALE, R.v[2][c] * W_FP8_SCALE, R.v[3][c] * W_FP8_SCALE); } }
.Lcv_j1_1:
	v_mul_f32_e32 v72, 0x43800000, v18
	v_mul_f32_e32 v93, 0x43800000, v22
	v_med3_f32 v72, v72, s31, v87
	v_med3_f32 v93, v93, s31, v87
	v_cvt_pk_fp8_f32 v95, v72, v93
	v_mul_f32_e32 v94, 0x43800000, v26
	v_mul_f32_e32 v72, 0x43800000, v30
	v_med3_f32 v93, v94, s31, v87
	v_med3_f32 v72, v72, s31, v87
	v_cvt_pk_fp8_f32 v95, v93, v72 op_sel:[0,0,1]
	s_lshl_b32 s36, s36, 13
	s_add_i32 s36, s36, 0
	v_add3_u32 v72, s36, v80, v88
	ds_write_b32 v72, v95
	v_mul_f32_e32 v72, 0x43800000, v19
	v_mul_f32_e32 v93, 0x43800000, v23
	v_med3_f32 v72, v72, s31, v87
	v_med3_f32 v93, v93, s31, v87
	v_cvt_pk_fp8_f32 v95, v72, v93
	v_mul_f32_e32 v94, 0x43800000, v27
	v_mul_f32_e32 v72, 0x43800000, v31
	v_med3_f32 v93, v94, s31, v87
	v_med3_f32 v72, v72, s31, v87
	v_cvt_pk_fp8_f32 v95, v93, v72 op_sel:[0,0,1]
	v_mul_f32_e32 v72, 0x43800000, v20
	v_mul_f32_e32 v93, 0x43800000, v24
	v_med3_f32 v72, v72, s31, v87
	v_med3_f32 v93, v93, s31, v87
	v_cvt_pk_fp8_f32 v96, v72, v93
	v_mul_f32_e32 v94, 0x43800000, v28
	v_mul_f32_e32 v72, 0x43800000, v32
	v_med3_f32 v93, v94, s31, v87
	v_med3_f32 v72, v72, s31, v87
	v_cvt_pk_fp8_f32 v96, v93, v72 op_sel:[0,0,1]
	v_add3_u32 v72, s36, v81, v89
	ds_write_b32 v72, v95
	v_add3_u32 v72, s36, v82, v90
	ds_write_b32 v72, v96
	v_mul_f32_e32 v72, 0x43800000, v21
	v_mul_f32_e32 v93, 0x43800000, v25
	v_med3_f32 v72, v72, s31, v87
	v_med3_f32 v93, v93, s31, v87
	v_cvt_pk_fp8_f32 v95, v72, v93
	v_mul_f32_e32 v94, 0x43800000, v29
	v_mul_f32_e32 v72, 0x43800000, v33
	v_med3_f32 v93, v94, s31, v87
	v_med3_f32 v72, v72, s31, v87
	v_cvt_pk_fp8_f32 v95, v93, v72 op_sel:[0,0,1]
	s_add_i32 s37, s19, s34
	v_add3_u32 v72, s36, v83, v91
	s_cmpk_gt_i32 s37, 0x7fff
	ds_write_b32 v72, v95
	s_cbranch_scc1 .LBB0_194
	s_ashr_i32 s38, s37, 31
	s_lshr_b32 s38, s38, 22
	s_add_i32 s39, s37, s38
	s_ashr_i32 s38, s39, 10
	s_and_b32 s39, s39, 0xfc00
	s_sub_i32 s37, s37, s39
	s_ashr_i32 s39, s38, 31
	s_lshl_b64 s[38:39], s[38:39], 25
	v_lshl_add_u64 v[18:19], v[66:67], 0, s[38:39]
	s_sext_i32_i16 s38, s37
	s_bfe_u32 s38, s38, 0x4001b
	s_add_i32 s38, s37, s38
	s_sext_i32_i16 s39, s38
	s_and_b32 s38, s38, 0xfff0
	s_sub_i32 s37, s37, s38
	s_lshl_b32 s38, s39, 2
	s_sext_i32_i16 s37, s37
	s_andn2_b32 s38, s38, 63
	v_lshl_add_u32 v26, s37, 7, v86
	s_ashr_i32 s39, s38, 31
	v_lshl_add_u64 v[18:19], s[38:39], 2, v[18:19]
	v_lshlrev_b32_e32 v72, 2, v68
	v_ashrrev_i32_e32 v27, 31, v26
	v_lshl_add_u64 v[28:29], v[18:19], 0, v[72:73]
	v_lshlrev_b64 v[18:19], 14, v[26:27]
	v_or_b32_e32 v20, 1, v26
	v_or_b32_e32 v30, 2, v26
	v_or_b32_e32 v26, 3, v26
	v_ashrrev_i32_e32 v21, 31, v20
	v_ashrrev_i32_e32 v31, 31, v30
	v_ashrrev_i32_e32 v27, 31, v26
	v_lshlrev_b64 v[20:21], 14, v[20:21]
	v_lshlrev_b64 v[30:31], 14, v[30:31]
	v_lshlrev_b64 v[26:27], 14, v[26:27]
	v_lshl_add_u64 v[18:19], v[28:29], 0, v[18:19]
	v_lshl_add_u64 v[22:23], v[28:29], 0, v[20:21]
	v_lshl_add_u64 v[30:31], v[28:29], 0, v[30:31]
	v_lshl_add_u64 v[32:33], v[28:29], 0, v[26:27]
	global_load_dwordx4 v[18:21], v[18:19], off sc1 nt
	s_nop 0
	global_load_dwordx4 v[22:25], v[22:23], off sc1 nt
	s_nop 0
	global_load_dwordx4 v[26:29], v[30:31], off sc1 nt
	s_nop 0
	global_load_dwordx4 v[30:33], v[32:33], off sc1 nt

; #define LAS __attribute__((address_space(3)))
; __device__ __forceinline__ void ttb_put(const TReg& R, LAS unsigned* tile, int tid) {
;     const int kr = tid >> 4, nq = tid & 15;
; #pragma unroll
;     for (int c = 0; c < 4; ++c) { const int n = 4 * nq + c;
;         tile[n * 32 + (kr ^ (n & 31))] = pk4_fp8(R.v[0][c] * W_FP8_SCALE, R.v[1][c] * W_FP8_SCALE, R.v[2][c] * W_FP8_SCALE, R.v[3][c] * W_FP8_SCALE); } }
.Lcv_j1_2:
	v_mul_f32_e32 v72, 0x43800000, v34
	v_mul_f32_e32 v93, 0x43800000, v38
	v_med3_f32 v72, v72, s31, v87
	v_med3_f32 v93, v93, s31, v87
	v_cvt_pk_fp8_f32 v95, v72, v93
	v_mul_f32_e32 v94, 0x43800000, v42
	v_mul_f32_e32 v72, 0x43800000, v46
	v_med3_f32 v93, v94, s31, v87
	v_med3_f32 v72, v72, s31, v87
	v_cvt_pk_fp8_f32 v95, v93, v72 op_sel:[0,0,1]
	s_lshl_b32 s35, s27, 13
	s_add_i32 s35, s35, 0
	v_add3_u32 v72, s35, v80, v88
	ds_write_b32 v72, v95
	v_mul_f32_e32 v72, 0x43800000, v35
	v_mul_f32_e32 v93, 0x43800000, v39
	v_med3_f32 v72, v72, s31, v87
	v_med3_f32 v93, v93, s31, v87
	v_cvt_pk_fp8_f32 v95, v72, v93
	v_mul_f32_e32 v94, 0x43800000, v43
	v_mul_f32_e32 v72, 0x43800000, v47
	v_med3_f32 v93, v94, s31, v87
	v_med3_f32 v72, v72, s31, v87
	v_cvt_pk_fp8_f32 v95, v93, v72 op_sel:[0,0,1]
	v_mul_f32_e32 v72, 0x43800000, v36
	v_mul_f32_e32 v93, 0x43800000, v40
	v_med3_f32 v72, v72, s31, v87
	v_med3_f32 v93, v93, s31, v87
	v_cvt_pk_fp8_f32 v96, v72, v93
	v_mul_f32_e32 v94, 0x43800000, v44
	v_mul_f32_e32 v72, 0x43800000, v48
	v_med3_f32 v93, v94, s31, v87
	v_med3_f32 v72, v72, s31, v87
	v_cvt_pk_fp8_f32 v96, v93, v72 op_sel:[0,0,1]
	v_add3_u32 v72, s35, v81, v89
	ds_write_b32 v72, v95
	v_add3_u32 v72, s35, v82, v90
	ds_write_b32 v72, v96
	v_mul_f32_e32 v72, 0x43800000, v37
	v_mul_f32_e32 v93, 0x43800000, v41
	v_med3_f32 v72, v72, s31, v87
	v_med3_f32 v93, v93, s31, v87
	v_cvt_pk_fp8_f32 v95, v72, v93
	v_mul_f32_e32 v94, 0x43800000, v45
	v_mul_f32_e32 v72, 0x43800000, v49
	v_med3_f32 v93, v94, s31, v87
	v_med3_f32 v72, v72, s31, v87
	v_cvt_pk_fp8_f32 v95, v93, v72 op_sel:[0,0,1]
	s_add_i32 s37, s18, s34
	v_add3_u32 v72, s35, v83, v91
	s_cmpk_gt_i32 s37, 0x7fff
	ds_write_b32 v72, v95
	s_cbranch_scc1 .LBB0_198
	s_ashr_i32 s38, s37, 31
	s_lshr_b32 s38, s38, 22
	s_add_i32 s39, s37, s38
	s_ashr_i32 s38, s39, 10
	s_and_b32 s39, s39, 0xfc00
	s_sub_i32 s37, s37, s39
	s_ashr_i32 s39, s38, 31
	s_lshl_b64 s[38:39], s[38:39], 25
	v_lshl_add_u64 v[34:35], v[66:67], 0, s[38:39]
	s_sext_i32_i16 s38, s37
	s_bfe_u32 s38, s38, 0x4001b
	s_add_i32 s38, s37, s38
	s_sext_i32_i16 s39, s38
	s_and_b32 s38, s38, 0xfff0
	s_sub_i32 s37, s37, s38
	s_lshl_b32 s38, s39, 2
	s_sext_i32_i16 s37, s37
	s_andn2_b32 s38, s38, 63
	v_lshl_add_u32 v42, s37, 7, v86
	s_ashr_i32 s39, s38, 31
	v_lshl_add_u64 v[34:35], s[38:39], 2, v[34:35]
	v_lshlrev_b32_e32 v72, 2, v68
	v_ashrrev_i32_e32 v43, 31, v42
	v_lshl_add_u64 v[44:45], v[34:35], 0, v[72:73]
	v_lshlrev_b64 v[34:35], 14, v[42:43]
	v_or_b32_e32 v36, 1, v42
	v_or_b32_e32 v46, 2, v42
	v_or_b32_e32 v42, 3, v42
	v_ashrrev_i32_e32 v37, 31, v36
	v_ashrrev_i32_e32 v47, 31, v46
	v_ashrrev_i32_e32 v43, 31, v42
	v_lshlrev_b64 v[36:37], 14, v[36:37]
	v_lshlrev_b64 v[46:47], 14, v[46:47]
	v_lshlrev_b64 v[42:43], 14, v[42:43]
	v_lshl_add_u64 v[34:35], v[44:45], 0, v[34:35]
	v_lshl_add_u64 v[38:39], v[44:45], 0, v[36:37]
	v_lshl_add_u64 v[46:47], v[44:45], 0, v[46:47]
	v_lshl_add_u64 v[48:49], v[44:45], 0, v[42:43]
	global_load_dwordx4 v[34:37], v[34:35], off sc1 nt
	s_nop 0
	global_load_dwordx4 v[38:41], v[38:39], off sc1 nt
	s_nop 0
	global_load_dwordx4 v[42:45], v[46:47], off sc1 nt
	s_nop 0
	global_load_dwordx4 v[46:49], v[48:49], off sc1 nt

; #define LAS __attribute__((address_space(3)))
; #define TB_LOAD(R_, t_) do { const int _t = (t_); if (_t < tot) { const int _b = _t / per, _r = _t % per; ttb_load(R_, src + (size_t)_b * K_ * N_, N_, (_r % kt) * 128, (_r / kt) * 64, C.tid); } } while (0)
; __device__ __forceinline__ void ttb_put(const TReg& R, LAS unsigned* tile, int tid) {
;     const int kr = tid >> 4, nq = tid & 15;
; #pragma unroll
;     for (int c = 0; c < 4; ++c) { const int n = 4 * nq + c;
;         tile[n * 32 + (kr ^ (n & 31))] = pk4_fp8(R.v[0][c] * W_FP8_SCALE, R.v[1][c] * W_FP8_SCALE, R.v[2][c] * W_FP8_SCALE, R.v[3][c] * W_FP8_SCALE); } }
; template <int K_, int N_, int MAP_> __device__ __forceinline__ void tjob_b(const Ctx& C, int bid, int G, const float* src, unsigned char* dstb, int nbatch) {
;     constexpr int kt = K_ / 128, ntile = N_ / 64, per = kt * ntile; const int tot = per * nbatch;
;     TReg R0, R1, R2, R3; int kbuf = 0;
;     ...
;     TB_LOAD(R0, bid); TB_LOAD(R1, bid + G); TB_LOAD(R2, bid + 2 * G); TB_LOAD(R3, bid + 3 * G);
.Lcv_j1_3:
	v_mul_f32_e32 v72, 0x43800000, v50
	v_mul_f32_e32 v93, 0x43800000, v54
	v_med3_f32 v72, v72, s31, v87
	v_med3_f32 v93, v93, s31, v87
	v_cvt_pk_fp8_f32 v95, v72, v93
	v_mul_f32_e32 v94, 0x43800000, v58
	v_mul_f32_e32 v72, 0x43800000, v62
	v_med3_f32 v93, v94, s31, v87
	v_med3_f32 v72, v72, s31, v87
	v_cvt_pk_fp8_f32 v95, v93, v72 op_sel:[0,0,1]
	s_lshl_b32 s35, s27, 13
	s_add_i32 s35, s35, 0
	v_add3_u32 v72, s35, v80, v88
	ds_write_b32 v72, v95
	v_mul_f32_e32 v72, 0x43800000, v51
	v_mul_f32_e32 v93, 0x43800000, v55
	v_med3_f32 v72, v72, s31, v87
	v_med3_f32 v93, v93, s31, v87
	v_cvt_pk_fp8_f32 v95, v72, v93
	v_mul_f32_e32 v94, 0x43800000, v59
	v_mul_f32_e32 v72, 0x43800000, v63
	v_med3_f32 v93, v94, s31, v87
	v_med3_f32 v72, v72, s31, v87
	v_cvt_pk_fp8_f32 v95, v93, v72 op_sel:[0,0,1]
	v_mul_f32_e32 v72, 0x43800000, v52
	v_mul_f32_e32 v93, 0x43800000, v56
	v_med3_f32 v72, v72, s31, v87
	v_med3_f32 v93, v93, s31, v87
	v_cvt_pk_fp8_f32 v96, v72, v93
	v_mul_f32_e32 v94, 0x43800000, v60
	v_mul_f32_e32 v72, 0x43800000, v64
	v_med3_f32 v93, v94, s31, v87
	v_med3_f32 v72, v72, s31, v87
	v_cvt_pk_fp8_f32 v96, v93, v72 op_sel:[0,0,1]
	v_add3_u32 v72, s35, v81, v89
	ds_write_b32 v72, v95
	v_add3_u32 v72, s35, v82, v90
	ds_write_b32 v72, v96
	v_mul_f32_e32 v72, 0x43800000, v53
	v_mul_f32_e32 v93, 0x43800000, v57
	v_med3_f32 v72, v72, s31, v87
	v_med3_f32 v93, v93, s31, v87
	v_cvt_pk_fp8_f32 v95, v72, v93
	v_mul_f32_e32 v94, 0x43800000, v61
	v_mul_f32_e32 v72, 0x43800000, v65
	v_med3_f32 v93, v94, s31, v87
	v_med3_f32 v72, v72, s31, v87
	v_cvt_pk_fp8_f32 v95, v93, v72 op_sel:[0,0,1]
	s_add_i32 s34, s17, s34
	v_add3_u32 v72, s35, v83, v91
	s_cmpk_gt_i32 s34, 0x7fff
	ds_write_b32 v72, v95
	s_cbranch_scc1 .LBB0_187
	s_ashr_i32 s37, s34, 31
	s_lshr_b32 s37, s37, 22
	s_add_i32 s37, s34, s37
	s_ashr_i32 s38, s37, 10
	s_and_b32 s37, s37, 0xfc00
	s_sub_i32 s34, s34, s37
	s_sext_i32_i16 s37, s34
	s_ashr_i32 s39, s38, 31
	s_bfe_u32 s37, s37, 0x4001b
	s_lshl_b64 s[38:39], s[38:39], 25
	s_add_i32 s37, s34, s37
	v_lshl_add_u64 v[50:51], v[66:67], 0, s[38:39]
	s_sext_i32_i16 s38, s37
	s_and_b32 s37, s37, 0xfff0
	s_sub_i32 s34, s34, s37
	s_lshl_b32 s37, s38, 2
	s_sext_i32_i16 s34, s34
	s_and_b32 s38, s37, 0xffffffc0
	v_lshl_add_u32 v58, s34, 7, v86
	s_ashr_i32 s39, s38, 31
	v_lshl_add_u64 v[50:51], s[38:39], 2, v[50:51]
	v_lshlrev_b32_e32 v72, 2, v68
	v_ashrrev_i32_e32 v59, 31, v58
	v_lshl_add_u64 v[60:61], v[50:51], 0, v[72:73]
	v_lshlrev_b64 v[50:51], 14, v[58:59]
	v_or_b32_e32 v52, 1, v58
	v_or_b32_e32 v62, 2, v58
	v_or_b32_e32 v58, 3, v58
	v_ashrrev_i32_e32 v53, 31, v52
	v_ashrrev_i32_e32 v63, 31, v62
	v_ashrrev_i32_e32 v59, 31, v58
	v_lshlrev_b64 v[52:53], 14, v[52:53]
	v_lshlrev_b64 v[62:63], 14, v[62:63]
	v_lshlrev_b64 v[58:59], 14, v[58:59]
	v_lshl_add_u64 v[50:51], v[60:61], 0, v[50:51]
	v_lshl_add_u64 v[54:55], v[60:61], 0, v[52:53]
	v_lshl_add_u64 v[62:63], v[60:61], 0, v[62:63]
	v_lshl_add_u64 v[64:65], v[60:61], 0, v[58:59]
	global_load_dwordx4 v[50:53], v[50:51], off sc1 nt
	s_nop 0
	global_load_dwordx4 v[54:57], v[54:55], off sc1 nt
	s_nop 0
	global_load_dwordx4 v[58:61], v[62:63], off sc1 nt
	s_nop 0
	global_load_dwordx4 v[62:65], v[64:65], off sc1 nt
	s_branch .LBB0_187
.LBB0_202:
	s_waitcnt vmcnt(0) lgkmcnt(0)
	v_mov_b64_e32 v[2:3], s[70:71]
	s_barrier
	flat_load_dwordx2 v[66:67], v[2:3] offset:200
	s_movk_i32 s8, 0x4000
	s_and_b64 s[6:7], s[2:3], exec
	s_cselect_b32 s25, s8, 0x2a00
	s_cmp_lt_i32 s1, s25
	s_cselect_b64 s[6:7], -1, 0
	s_cmp_ge_i32 s1, s25
	s_cbranch_scc1 .LBB0_204
	s_ashr_i32 s8, s1, 31
	s_lshr_b32 s8, s8, 23
	s_add_i32 s9, s1, s8
	s_ashr_i32 s8, s9, 9
	s_and_b32 s9, s9, 0xfe00
	s_sub_i32 s12, s1, s9
	s_sext_i32_i16 s13, s12
	s_bfe_u32 s13, s13, 0x4001b
	s_add_i32 s13, s12, s13
	s_sext_i32_i16 s26, s13
	s_and_b32 s13, s13, 0xfff0
	s_sub_i32 s12, s12, s13
	s_ashr_i32 s9, s8, 31
	s_sext_i32_i16 s27, s12
	s_lshl_b32 s12, s26, 2
	s_lshl_b64 s[8:9], s[8:9], 24
	s_andn2_b32 s12, s12, 63
	v_and_b32_e32 v4, -4, v69
	s_ashr_i32 s13, s12, 31
	s_waitcnt vmcnt(0) lgkmcnt(0)
	v_lshl_add_u64 v[2:3], v[66:67], 0, s[8:9]
	v_lshl_add_u32 v10, s27, 7, v4
	v_lshl_add_u64 v[2:3], s[12:13], 2, v[2:3]
	v_and_b32_e32 v4, 0xf0, v74
	v_mov_b32_e32 v5, 0
	v_ashrrev_i32_e32 v11, 31, v10
	v_lshl_add_u64 v[12:13], v[2:3], 0, v[4:5]
	v_lshlrev_b64 v[2:3], 13, v[10:11]
	v_lshl_add_u64 v[14:15], v[12:13], 0, v[2:3]
	v_or_b32_e32 v2, 1, v10
	v_ashrrev_i32_e32 v3, 31, v2
	v_lshlrev_b64 v[2:3], 13, v[2:3]
	v_lshl_add_u64 v[16:17], v[12:13], 0, v[2:3]
	global_load_dwordx4 v[2:5], v[14:15], off sc1 nt
	global_load_dwordx4 v[6:9], v[16:17], off sc1 nt
	v_or_b32_e32 v14, 2, v10
	v_ashrrev_i32_e32 v15, 31, v14
	v_or_b32_e32 v10, 3, v10
	v_lshlrev_b64 v[14:15], 13, v[14:15]
	v_ashrrev_i32_e32 v11, 31, v10
	v_lshl_add_u64 v[18:19], v[12:13], 0, v[14:15]
	v_lshlrev_b64 v[10:11], 13, v[10:11]
	v_lshl_add_u64 v[20:21], v[12:13], 0, v[10:11]
	global_load_dwordx4 v[10:13], v[18:19], off sc1 nt
	global_load_dwordx4 v[14:17], v[20:21], off sc1 nt
; #define LAS __attribute__((address_space(3)))
; #define TB_LOAD(R_, t_) do { const int _t = (t_); if (_t < tot) { const int _b = _t / per, _r = _t % per; ttb_load(R_, src + (size_t)_b * K_ * N_, N_, (_r % kt) * 128, (_r / kt) * 64, C.tid); } } while (0)
; __device__ __forceinline__ void ttb_load(TReg& R, const float* src, int ld, int k0, int n0, int tid) {
;     const int kr = tid >> 4, nq = tid & 15;
; #pragma unroll
;     for (int rep = 0; rep < 4; ++rep) R.v[rep] = __builtin_nontemporal_load((const f32x4*)(src + (size_t)(k0 + 4 * kr + rep) * ld + n0 + 4 * nq)); }
; __device__ __forceinline__ void ttb_put(const TReg& R, LAS unsigned* tile, int tid) {
;     const int kr = tid >> 4, nq = tid & 15;
; #pragma unroll
;     for (int c = 0; c < 4; ++c) { const int n = 4 * nq + c;
;         tile[n * 32 + (kr ^ (n & 31))] = pk4_fp8(R.v[0][c] * W_FP8_SCALE, R.v[1][c] * W_FP8_SCALE, R.v[2][c] * W_FP8_SCALE, R.v[3][c] * W_FP8_SCALE); } }
; __device__ __forceinline__ void ttb_finish(LAS const unsigned* tile, unsigned char* dst, int ldd, int k0, int n0, int map, int tid) {
;     const int n = tid >> 3, kq = tid & 7, m = n & 31, ns = n0 + n; int r = ns;
;     if (map == 2) { const int j = ns >> 1, par = ns & 1; r = 256 * (j >> 7) + 128 * par + (j & 127); }
;     const u32x4 g = *(LAS const u32x4*)(tile + n * 32 + 4 * (kq ^ (m >> 2)));
;     const unsigned a0 = (m & 1) ? g.y : g.x, a1 = (m & 1) ? g.x : g.y, a2 = (m & 1) ? g.w : g.z, a3 = (m & 1) ? g.z : g.w;
;     u32x4 w; w.x = (m & 2) ? a2 : a0; w.y = (m & 2) ? a3 : a1; w.z = (m & 2) ? a0 : a2; w.w = (m & 2) ? a1 : a3;
;     __builtin_nontemporal_store(w, (u32x4*)(dst + (size_t)r * ldd + k0 + 16 * kq));
; }
; template <int K_, int N_, int MAP_> __device__ __forceinline__ void tjob_b(const Ctx& C, int bid, int G, const float* src, unsigned char* dstb, int nbatch) {
;     constexpr int kt = K_ / 128, ntile = N_ / 64, per = kt * ntile; const int tot = per * nbatch;
;     TReg R0, R1, R2, R3; int kbuf = 0;
;     ...
;     TB_LOAD(R0, bid); TB_LOAD(R1, bid + G); TB_LOAD(R2, bid + 2 * G); TB_LOAD(R3, bid + 3 * G);
.LBB0_204:
	s_cmp_ge_i32 s22, s25
	s_cbranch_scc1 .LBB0_206
	s_ashr_i32 s8, s22, 31
	s_lshr_b32 s8, s8, 23
	s_add_i32 s9, s22, s8
	s_ashr_i32 s8, s9, 9
	s_and_b32 s9, s9, 0xfe00
	s_sub_i32 s12, s22, s9
	s_sext_i32_i16 s13, s12
	s_bfe_u32 s13, s13, 0x4001b
	s_add_i32 s13, s12, s13
	s_sext_i32_i16 s22, s13
	s_and_b32 s13, s13, 0xfff0
	s_sub_i32 s12, s12, s13
	s_ashr_i32 s9, s8, 31
	s_sext_i32_i16 s26, s12
	s_lshl_b32 s12, s22, 2
	s_lshl_b64 s[8:9], s[8:9], 24
	s_andn2_b32 s12, s12, 63
	v_and_b32_e32 v20, -4, v69
	s_ashr_i32 s13, s12, 31
	s_waitcnt vmcnt(0) lgkmcnt(0)
	v_lshl_add_u64 v[18:19], v[66:67], 0, s[8:9]
	v_lshl_add_u32 v26, s26, 7, v20
	v_lshl_add_u64 v[18:19], s[12:13], 2, v[18:19]
	v_and_b32_e32 v20, 0xf0, v74
	v_mov_b32_e32 v21, 0
	v_ashrrev_i32_e32 v27, 31, v26
	v_lshl_add_u64 v[28:29], v[18:19], 0, v[20:21]
	v_lshlrev_b64 v[18:19], 13, v[26:27]
	v_lshl_add_u64 v[30:31], v[28:29], 0, v[18:19]
	v_or_b32_e32 v18, 1, v26
	v_ashrrev_i32_e32 v19, 31, v18
	v_lshlrev_b64 v[18:19], 13, v[18:19]
	v_lshl_add_u64 v[32:33], v[28:29], 0, v[18:19]
	global_load_dwordx4 v[18:21], v[30:31], off sc1 nt
	global_load_dwordx4 v[22:25], v[32:33], off sc1 nt
	v_or_b32_e32 v30, 2, v26
	v_ashrrev_i32_e32 v31, 31, v30
	v_or_b32_e32 v26, 3, v26
	v_lshlrev_b64 v[30:31], 13, v[30:31]
	v_ashrrev_i32_e32 v27, 31, v26
	v_lshl_add_u64 v[34:35], v[28:29], 0, v[30:31]
	v_lshlrev_b64 v[26:27], 13, v[26:27]
	v_lshl_add_u64 v[36:37], v[28:29], 0, v[26:27]
	global_load_dwordx4 v[26:29], v[34:35], off sc1 nt
	global_load_dwordx4 v[30:33], v[36:37], off sc1 nt
.LBB0_206:
	s_cmp_ge_i32 s23, s25
	s_cbranch_scc1 .LBB0_208
	s_ashr_i32 s8, s23, 31
	s_lshr_b32 s8, s8, 23
	s_add_i32 s9, s23, s8
	s_ashr_i32 s8, s9, 9
	s_and_b32 s9, s9, 0xfe00
	s_sub_i32 s12, s23, s9
	s_sext_i32_i16 s13, s12
	s_bfe_u32 s13, s13, 0x4001b
	s_add_i32 s13, s12, s13
	s_sext_i32_i16 s22, s13
	s_and_b32 s13, s13, 0xfff0
	s_sub_i32 s12, s12, s13
	s_ashr_i32 s9, s8, 31
	s_sext_i32_i16 s23, s12
	s_lshl_b32 s12, s22, 2
	s_lshl_b64 s[8:9], s[8:9], 24
	s_andn2_b32 s12, s12, 63
	v_and_b32_e32 v36, -4, v69
	s_ashr_i32 s13, s12, 31
	s_waitcnt vmcnt(0) lgkmcnt(0)
	v_lshl_add_u64 v[34:35], v[66:67], 0, s[8:9]
	v_lshl_add_u32 v42, s23, 7, v36
	v_lshl_add_u64 v[34:35], s[12:13], 2, v[34:35]
	v_and_b32_e32 v36, 0xf0, v74
	v_mov_b32_e32 v37, 0
	v_ashrrev_i32_e32 v43, 31, v42
	v_lshl_add_u64 v[44:45], v[34:35], 0, v[36:37]
	v_lshlrev_b64 v[34:35], 13, v[42:43]
	v_lshl_add_u64 v[46:47], v[44:45], 0, v[34:35]
	v_or_b32_e32 v34, 1, v42
	v_ashrrev_i32_e32 v35, 31, v34
	v_lshlrev_b64 v[34:35], 13, v[34:35]
	v_lshl_add_u64 v[48:49], v[44:45], 0, v[34:35]
	global_load_dwordx4 v[34:37], v[46:47], off sc1 nt
	global_load_dwordx4 v[38:41], v[48:49], off sc1 nt
	v_or_b32_e32 v46, 2, v42
	v_ashrrev_i32_e32 v47, 31, v46
	v_or_b32_e32 v42, 3, v42
	v_lshlrev_b64 v[46:47], 13, v[46:47]
	v_ashrrev_i32_e32 v43, 31, v42
	v_lshl_add_u64 v[50:51], v[44:45], 0, v[46:47]
	v_lshlrev_b64 v[42:43], 13, v[42:43]
	v_lshl_add_u64 v[52:53], v[44:45], 0, v[42:43]
	global_load_dwordx4 v[42:45], v[50:51], off sc1 nt
	global_load_dwordx4 v[46:49], v[52:53], off sc1 nt
.LBB0_208:
	s_cmp_ge_i32 s24, s25
	s_cbranch_scc1 .LBB0_210
	s_ashr_i32 s8, s24, 31
	s_lshr_b32 s8, s8, 23
	s_add_i32 s9, s24, s8
	s_ashr_i32 s8, s9, 9
	s_and_b32 s9, s9, 0xfe00
	s_sub_i32 s12, s24, s9
	s_sext_i32_i16 s13, s12
	s_bfe_u32 s13, s13, 0x4001b
	s_add_i32 s13, s12, s13
	s_sext_i32_i16 s22, s13
	s_and_b32 s13, s13, 0xfff0
	s_sub_i32 s12, s12, s13
	s_ashr_i32 s9, s8, 31
	s_sext_i32_i16 s23, s12
	s_lshl_b32 s12, s22, 2
	s_lshl_b64 s[8:9], s[8:9], 24
	s_andn2_b32 s12, s12, 63
	v_and_b32_e32 v52, -4, v69
	s_ashr_i32 s13, s12, 31
	s_waitcnt vmcnt(0) lgkmcnt(0)
	v_lshl_add_u64 v[50:51], v[66:67], 0, s[8:9]
	v_lshl_add_u32 v58, s23, 7, v52
	v_lshl_add_u64 v[50:51], s[12:13], 2, v[50:51]
	v_and_b32_e32 v52, 0xf0, v74
	v_mov_b32_e32 v53, 0
	v_ashrrev_i32_e32 v59, 31, v58
	v_lshl_add_u64 v[60:61], v[50:51], 0, v[52:53]
	v_lshlrev_b64 v[50:51], 13, v[58:59]
	v_lshl_add_u64 v[62:63], v[60:61], 0, v[50:51]
	v_or_b32_e32 v50, 1, v58
	v_ashrrev_i32_e32 v51, 31, v50
	v_lshlrev_b64 v[50:51], 13, v[50:51]
	v_lshl_add_u64 v[64:65], v[60:61], 0, v[50:51]
	global_load_dwordx4 v[50:53], v[62:63], off sc1 nt
	global_load_dwordx4 v[54:57], v[64:65], off sc1 nt
	v_or_b32_e32 v62, 2, v58
	v_ashrrev_i32_e32 v63, 31, v62
	v_or_b32_e32 v58, 3, v58
	v_lshlrev_b64 v[62:63], 13, v[62:63]
	v_ashrrev_i32_e32 v59, 31, v58
	v_lshl_add_u64 v[70:71], v[60:61], 0, v[62:63]
	v_lshlrev_b64 v[58:59], 13, v[58:59]
	v_lshl_add_u64 v[72:73], v[60:61], 0, v[58:59]
	global_load_dwordx4 v[58:61], v[70:71], off sc1 nt
	global_load_dwordx4 v[62:65], v[72:73], off sc1 nt
	s_andn2_b64 vcc, exec, s[6:7]
	s_cbranch_vccnz .LBB0_227
	s_branch .LBB0_211

; #define LAS __attribute__((address_space(3)))
; __device__ __forceinline__ void ttb_put(const TReg& R, LAS unsigned* tile, int tid) {
;     const int kr = tid >> 4, nq = tid & 15;
; #pragma unroll
;     for (int c = 0; c < 4; ++c) { const int n = 4 * nq + c;
;         tile[n * 32 + (kr ^ (n & 31))] = pk4_fp8(R.v[0][c] * W_FP8_SCALE, R.v[1][c] * W_FP8_SCALE, R.v[2][c] * W_FP8_SCALE, R.v[3][c] * W_FP8_SCALE); } }
.Lcv_j2_0:
	v_mul_f32_e32 v72, 0x43800000, v2
	v_mul_f32_e32 v85, 0x43800000, v6
	v_med3_f32 v72, v72, s26, v75
	v_med3_f32 v85, v85, s26, v75
	v_cvt_pk_fp8_f32 v87, v72, v85
	v_mul_f32_e32 v86, 0x43800000, v10
	v_mul_f32_e32 v72, 0x43800000, v14
	v_med3_f32 v85, v86, s26, v75
	v_med3_f32 v72, v72, s26, v75
	v_cvt_pk_fp8_f32 v87, v85, v72 op_sel:[0,0,1]
	v_mul_f32_e32 v72, 0x43800000, v3
	v_mul_f32_e32 v85, 0x43800000, v7
	v_med3_f32 v72, v72, s26, v75
	v_med3_f32 v85, v85, s26, v75
	v_cvt_pk_fp8_f32 v88, v72, v85
	v_mul_f32_e32 v86, 0x43800000, v11
	v_mul_f32_e32 v72, 0x43800000, v15
	v_med3_f32 v85, v86, s26, v75
	v_med3_f32 v72, v72, s26, v75
	s_lshl_b32 s12, s24, 13
	v_cvt_pk_fp8_f32 v88, v85, v72 op_sel:[0,0,1]
	s_add_i32 s31, s12, 0
	v_add3_u32 v72, s31, v74, v76
	ds_write_b32 v72, v87
	v_add3_u32 v72, s31, v79, v77
	ds_write_b32 v72, v88
	v_mul_f32_e32 v72, 0x43800000, v4
	v_mul_f32_e32 v85, 0x43800000, v8
	v_med3_f32 v72, v72, s26, v75
	v_med3_f32 v85, v85, s26, v75
	v_cvt_pk_fp8_f32 v87, v72, v85
	v_mul_f32_e32 v86, 0x43800000, v12
	v_mul_f32_e32 v72, 0x43800000, v16
	v_med3_f32 v85, v86, s26, v75
	v_med3_f32 v72, v72, s26, v75
	v_cvt_pk_fp8_f32 v87, v85, v72 op_sel:[0,0,1]
	v_mul_f32_e32 v72, 0x43800000, v5
	v_mul_f32_e32 v85, 0x43800000, v9
	v_med3_f32 v72, v72, s26, v75
	v_med3_f32 v85, v85, s26, v75
	v_cvt_pk_fp8_f32 v88, v72, v85
	v_mul_f32_e32 v86, 0x43800000, v13
	v_mul_f32_e32 v72, 0x43800000, v17
	v_med3_f32 v85, v86, s26, v75
	v_med3_f32 v72, v72, s26, v75
	v_cvt_pk_fp8_f32 v88, v85, v72 op_sel:[0,0,1]
	s_add_i32 s27, s1, s16
	s_cmp_ge_i32 s27, s25
	v_add3_u32 v72, s31, v80, v82
	s_cselect_b64 s[12:13], -1, 0
	ds_write_b32 v72, v87
	v_add3_u32 v72, s31, v78, v83
	s_and_b64 vcc, exec, s[12:13]
	ds_write_b32 v72, v88
	s_cbranch_vccnz .LBB0_216
	s_ashr_i32 s33, s27, 31
	s_lshr_b32 s33, s33, 23
	s_add_i32 s33, s27, s33
	s_ashr_i32 s34, s33, 9
	s_and_b32 s33, s33, 0xfe00
	s_ashr_i32 s35, s34, 31
	s_sub_i32 s33, s27, s33
	s_lshl_b64 s[34:35], s[34:35], 24
	v_lshl_add_u64 v[2:3], v[66:67], 0, s[34:35]
	s_sext_i32_i16 s34, s33
	s_bfe_u32 s34, s34, 0x4001b
	s_add_i32 s34, s33, s34
	s_sext_i32_i16 s35, s34
	s_and_b32 s34, s34, 0xfff0
	s_sub_i32 s33, s33, s34
	s_lshl_b32 s34, s35, 2
	s_sext_i32_i16 s33, s33
	s_andn2_b32 s34, s34, 63
	v_lshl_add_u32 v10, s33, 7, v69
	s_ashr_i32 s35, s34, 31
	v_lshl_add_u64 v[2:3], s[34:35], 2, v[2:3]
	v_lshlrev_b32_e32 v72, 2, v68
	v_ashrrev_i32_e32 v11, 31, v10
	v_lshl_add_u64 v[12:13], v[2:3], 0, v[72:73]
	v_lshlrev_b64 v[2:3], 13, v[10:11]
	v_lshl_add_u64 v[14:15], v[12:13], 0, v[2:3]
	v_or_b32_e32 v2, 1, v10
	v_ashrrev_i32_e32 v3, 31, v2
	v_lshlrev_b64 v[2:3], 13, v[2:3]
	v_lshl_add_u64 v[16:17], v[12:13], 0, v[2:3]
	global_load_dwordx4 v[2:5], v[14:15], off sc1 nt
	global_load_dwordx4 v[6:9], v[16:17], off sc1 nt
	v_or_b32_e32 v14, 2, v10
	v_ashrrev_i32_e32 v15, 31, v14
	v_or_b32_e32 v10, 3, v10
	v_lshlrev_b64 v[14:15], 13, v[14:15]
	v_ashrrev_i32_e32 v11, 31, v10
	v_lshl_add_u64 v[86:87], v[12:13], 0, v[14:15]
	v_lshlrev_b64 v[10:11], 13, v[10:11]
	v_lshl_add_u64 v[88:89], v[12:13], 0, v[10:11]
	global_load_dwordx4 v[10:13], v[86:87], off sc1 nt
	global_load_dwordx4 v[14:17], v[88:89], off sc1 nt

; #define LAS __attribute__((address_space(3)))
; __device__ __forceinline__ void ttb_put(const TReg& R, LAS unsigned* tile, int tid) {
;     const int kr = tid >> 4, nq = tid & 15;
; #pragma unroll
;     for (int c = 0; c < 4; ++c) { const int n = 4 * nq + c;
;         tile[n * 32 + (kr ^ (n & 31))] = pk4_fp8(R.v[0][c] * W_FP8_SCALE, R.v[1][c] * W_FP8_SCALE, R.v[2][c] * W_FP8_SCALE, R.v[3][c] * W_FP8_SCALE); } }
.Lcv_j2_1:
	v_mul_f32_e32 v72, 0x43800000, v18
	v_mul_f32_e32 v85, 0x43800000, v22
	v_med3_f32 v72, v72, s26, v75
	v_med3_f32 v85, v85, s26, v75
	v_cvt_pk_fp8_f32 v87, v72, v85
	v_mul_f32_e32 v86, 0x43800000, v26
	v_mul_f32_e32 v72, 0x43800000, v30
	v_med3_f32 v85, v86, s26, v75
	v_med3_f32 v72, v72, s26, v75
	v_cvt_pk_fp8_f32 v87, v85, v72 op_sel:[0,0,1]
	s_lshl_b32 s33, s33, 13
	s_add_i32 s33, s33, 0
	v_add3_u32 v72, s33, v74, v76
	ds_write_b32 v72, v87
	v_mul_f32_e32 v72, 0x43800000, v19
	v_mul_f32_e32 v85, 0x43800000, v23
	v_med3_f32 v72, v72, s26, v75
	v_med3_f32 v85, v85, s26, v75
	v_cvt_pk_fp8_f32 v87, v72, v85
	v_mul_f32_e32 v86, 0x43800000, v27
	v_mul_f32_e32 v72, 0x43800000, v31
	v_med3_f32 v85, v86, s26, v75
	v_med3_f32 v72, v72, s26, v75
	v_cvt_pk_fp8_f32 v87, v85, v72 op_sel:[0,0,1]
	v_mul_f32_e32 v72, 0x43800000, v20
	v_mul_f32_e32 v85, 0x43800000, v24
	v_med3_f32 v72, v72, s26, v75
	v_med3_f32 v85, v85, s26, v75
	v_cvt_pk_fp8_f32 v88, v72, v85
	v_mul_f32_e32 v86, 0x43800000, v28
	v_mul_f32_e32 v72, 0x43800000, v32
	v_med3_f32 v85, v86, s26, v75
	v_med3_f32 v72, v72, s26, v75
	v_cvt_pk_fp8_f32 v88, v85, v72 op_sel:[0,0,1]
	v_add3_u32 v72, s33, v79, v77
	ds_write_b32 v72, v87
	v_add3_u32 v72, s33, v80, v82
	ds_write_b32 v72, v88
	v_mul_f32_e32 v72, 0x43800000, v21
	v_mul_f32_e32 v85, 0x43800000, v25
	v_med3_f32 v72, v72, s26, v75
	v_med3_f32 v85, v85, s26, v75
	v_cvt_pk_fp8_f32 v87, v72, v85
	v_mul_f32_e32 v86, 0x43800000, v29
	v_mul_f32_e32 v72, 0x43800000, v33
	v_med3_f32 v85, v86, s26, v75
	v_med3_f32 v72, v72, s26, v75
	v_cvt_pk_fp8_f32 v87, v85, v72 op_sel:[0,0,1]
	s_add_i32 s34, s19, s1
	v_add3_u32 v72, s33, v78, v83
	s_cmp_ge_i32 s34, s25
	ds_write_b32 v72, v87
	s_cbranch_scc1 .LBB0_219
	s_ashr_i32 s35, s34, 31
	s_lshr_b32 s35, s35, 23
	s_add_i32 s35, s34, s35
	s_ashr_i32 s36, s35, 9
	s_and_b32 s35, s35, 0xfe00
	s_ashr_i32 s37, s36, 31
	s_sub_i32 s38, s34, s35
	s_lshl_b64 s[34:35], s[36:37], 24
	v_lshl_add_u64 v[18:19], v[66:67], 0, s[34:35]
	s_sext_i32_i16 s34, s38
	s_bfe_u32 s34, s34, 0x4001b
	s_add_i32 s34, s38, s34
	s_sext_i32_i16 s35, s34
	s_and_b32 s34, s34, 0xfff0
	s_sub_i32 s34, s38, s34
	s_sext_i32_i16 s36, s34
	s_lshl_b32 s34, s35, 2
	s_andn2_b32 s34, s34, 63
	v_lshl_add_u32 v26, s36, 7, v69
	s_ashr_i32 s35, s34, 31
	v_lshl_add_u64 v[18:19], s[34:35], 2, v[18:19]
	v_lshlrev_b32_e32 v72, 2, v68
	v_ashrrev_i32_e32 v27, 31, v26
	v_lshl_add_u64 v[28:29], v[18:19], 0, v[72:73]
	v_lshlrev_b64 v[18:19], 13, v[26:27]
	v_lshl_add_u64 v[30:31], v[28:29], 0, v[18:19]
	v_or_b32_e32 v18, 1, v26
	v_ashrrev_i32_e32 v19, 31, v18
	v_lshlrev_b64 v[18:19], 13, v[18:19]
	v_lshl_add_u64 v[32:33], v[28:29], 0, v[18:19]
	global_load_dwordx4 v[18:21], v[30:31], off sc1 nt
	global_load_dwordx4 v[22:25], v[32:33], off sc1 nt
	v_or_b32_e32 v30, 2, v26
	v_ashrrev_i32_e32 v31, 31, v30
	v_or_b32_e32 v26, 3, v26
	v_lshlrev_b64 v[30:31], 13, v[30:31]
	v_ashrrev_i32_e32 v27, 31, v26
	v_lshl_add_u64 v[86:87], v[28:29], 0, v[30:31]
	v_lshlrev_b64 v[26:27], 13, v[26:27]
	v_lshl_add_u64 v[88:89], v[28:29], 0, v[26:27]
	global_load_dwordx4 v[26:29], v[86:87], off sc1 nt
	global_load_dwordx4 v[30:33], v[88:89], off sc1 nt

; #define LAS __attribute__((address_space(3)))
; __device__ __forceinline__ void ttb_put(const TReg& R, LAS unsigned* tile, int tid) {
;     const int kr = tid >> 4, nq = tid & 15;
; #pragma unroll
;     for (int c = 0; c < 4; ++c) { const int n = 4 * nq + c;
;         tile[n * 32 + (kr ^ (n & 31))] = pk4_fp8(R.v[0][c] * W_FP8_SCALE, R.v[1][c] * W_FP8_SCALE, R.v[2][c] * W_FP8_SCALE, R.v[3][c] * W_FP8_SCALE); } }
.Lcv_j2_2:
	v_mul_f32_e32 v72, 0x43800000, v34
	v_mul_f32_e32 v85, 0x43800000, v38
	v_med3_f32 v72, v72, s26, v75
	v_med3_f32 v85, v85, s26, v75
	v_cvt_pk_fp8_f32 v87, v72, v85
	v_mul_f32_e32 v86, 0x43800000, v42
	v_mul_f32_e32 v72, 0x43800000, v46
	v_med3_f32 v85, v86, s26, v75
	v_med3_f32 v72, v72, s26, v75
	v_cvt_pk_fp8_f32 v87, v85, v72 op_sel:[0,0,1]
	s_lshl_b32 s33, s24, 13
	s_add_i32 s33, s33, 0
	v_add3_u32 v72, s33, v74, v76
	ds_write_b32 v72, v87
	v_mul_f32_e32 v72, 0x43800000, v35
	v_mul_f32_e32 v85, 0x43800000, v39
	v_med3_f32 v72, v72, s26, v75
	v_med3_f32 v85, v85, s26, v75
	v_cvt_pk_fp8_f32 v87, v72, v85
	v_mul_f32_e32 v86, 0x43800000, v43
	v_mul_f32_e32 v72, 0x43800000, v47
	v_med3_f32 v85, v86, s26, v75
	v_med3_f32 v72, v72, s26, v75
	v_cvt_pk_fp8_f32 v87, v85, v72 op_sel:[0,0,1]
	v_mul_f32_e32 v72, 0x43800000, v36
	v_mul_f32_e32 v85, 0x43800000, v40
	v_med3_f32 v72, v72, s26, v75
	v_med3_f32 v85, v85, s26, v75
	v_cvt_pk_fp8_f32 v88, v72, v85
	v_mul_f32_e32 v86, 0x43800000, v44
	v_mul_f32_e32 v72, 0x43800000, v48
	v_med3_f32 v85, v86, s26, v75
	v_med3_f32 v72, v72, s26, v75
	v_cvt_pk_fp8_f32 v88, v85, v72 op_sel:[0,0,1]
	v_add3_u32 v72, s33, v79, v77
	ds_write_b32 v72, v87
	v_add3_u32 v72, s33, v80, v82
	ds_write_b32 v72, v88
	v_mul_f32_e32 v72, 0x43800000, v37
	v_mul_f32_e32 v85, 0x43800000, v41
	v_med3_f32 v72, v72, s26, v75
	v_med3_f32 v85, v85, s26, v75
	v_cvt_pk_fp8_f32 v87, v72, v85
	v_mul_f32_e32 v86, 0x43800000, v45
	v_mul_f32_e32 v72, 0x43800000, v49
	v_med3_f32 v85, v86, s26, v75
	v_med3_f32 v72, v72, s26, v75
	v_cvt_pk_fp8_f32 v87, v85, v72 op_sel:[0,0,1]
	s_add_i32 s34, s18, s1
	v_add3_u32 v72, s33, v78, v83
	s_cmp_ge_i32 s34, s25
	ds_write_b32 v72, v87
	s_cbranch_scc1 .LBB0_223
	s_ashr_i32 s35, s34, 31
	s_lshr_b32 s35, s35, 23
	s_add_i32 s35, s34, s35
	s_ashr_i32 s36, s35, 9
	s_and_b32 s35, s35, 0xfe00
	s_ashr_i32 s37, s36, 31
	s_sub_i32 s38, s34, s35
	s_lshl_b64 s[34:35], s[36:37], 24
	v_lshl_add_u64 v[34:35], v[66:67], 0, s[34:35]
	s_sext_i32_i16 s34, s38
	s_bfe_u32 s34, s34, 0x4001b
	s_add_i32 s34, s38, s34
	s_sext_i32_i16 s35, s34
	s_and_b32 s34, s34, 0xfff0
	s_sub_i32 s34, s38, s34
	s_sext_i32_i16 s36, s34
	s_lshl_b32 s34, s35, 2
	s_andn2_b32 s34, s34, 63
	v_lshl_add_u32 v42, s36, 7, v69
	s_ashr_i32 s35, s34, 31
	v_lshl_add_u64 v[34:35], s[34:35], 2, v[34:35]
	v_lshlrev_b32_e32 v72, 2, v68
	v_ashrrev_i32_e32 v43, 31, v42
	v_lshl_add_u64 v[44:45], v[34:35], 0, v[72:73]
	v_lshlrev_b64 v[34:35], 13, v[42:43]
	v_lshl_add_u64 v[46:47], v[44:45], 0, v[34:35]
	v_or_b32_e32 v34, 1, v42
	v_ashrrev_i32_e32 v35, 31, v34
	v_lshlrev_b64 v[34:35], 13, v[34:35]
	v_lshl_add_u64 v[48:49], v[44:45], 0, v[34:35]
	global_load_dwordx4 v[34:37], v[46:47], off sc1 nt
	global_load_dwordx4 v[38:41], v[48:49], off sc1 nt
	v_or_b32_e32 v46, 2, v42
	v_ashrrev_i32_e32 v47, 31, v46
	v_or_b32_e32 v42, 3, v42
	v_lshlrev_b64 v[46:47], 13, v[46:47]
	v_ashrrev_i32_e32 v43, 31, v42
	v_lshl_add_u64 v[86:87], v[44:45], 0, v[46:47]
	v_lshlrev_b64 v[42:43], 13, v[42:43]
	v_lshl_add_u64 v[88:89], v[44:45], 0, v[42:43]
	global_load_dwordx4 v[42:45], v[86:87], off sc1 nt
	global_load_dwordx4 v[46:49], v[88:89], off sc1 nt

; #define LAS __attribute__((address_space(3)))
; __device__ __forceinline__ void ttb_put(const TReg& R, LAS unsigned* tile, int tid) {
;     const int kr = tid >> 4, nq = tid & 15;
; #pragma unroll
;     for (int c = 0; c < 4; ++c) { const int n = 4 * nq + c;
;         tile[n * 32 + (kr ^ (n & 31))] = pk4_fp8(R.v[0][c] * W_FP8_SCALE, R.v[1][c] * W_FP8_SCALE, R.v[2][c] * W_FP8_SCALE, R.v[3][c] * W_FP8_SCALE); } }
.Lcv_j2_3:
	v_mul_f32_e32 v72, 0x43800000, v50
	v_mul_f32_e32 v85, 0x43800000, v54
	v_med3_f32 v72, v72, s26, v75
	v_med3_f32 v85, v85, s26, v75
	v_cvt_pk_fp8_f32 v87, v72, v85
	v_mul_f32_e32 v86, 0x43800000, v58
	v_mul_f32_e32 v72, 0x43800000, v62
	v_med3_f32 v85, v86, s26, v75
	v_med3_f32 v72, v72, s26, v75
	v_cvt_pk_fp8_f32 v87, v85, v72 op_sel:[0,0,1]
	s_lshl_b32 s33, s24, 13
	s_add_i32 s33, s33, 0
	v_add3_u32 v72, s33, v74, v76
	ds_write_b32 v72, v87
	v_mul_f32_e32 v72, 0x43800000, v51
	v_mul_f32_e32 v85, 0x43800000, v55
	v_med3_f32 v72, v72, s26, v75
	v_med3_f32 v85, v85, s26, v75
	v_cvt_pk_fp8_f32 v87, v72, v85
	v_mul_f32_e32 v86, 0x43800000, v59
	v_mul_f32_e32 v72, 0x43800000, v63
	v_med3_f32 v85, v86, s26, v75
	v_med3_f32 v72, v72, s26, v75
	v_cvt_pk_fp8_f32 v87, v85, v72 op_sel:[0,0,1]
	v_mul_f32_e32 v72, 0x43800000, v52
	v_mul_f32_e32 v85, 0x43800000, v56
	v_med3_f32 v72, v72, s26, v75
	v_med3_f32 v85, v85, s26, v75
	v_cvt_pk_fp8_f32 v88, v72, v85
	v_mul_f32_e32 v86, 0x43800000, v60
	v_mul_f32_e32 v72, 0x43800000, v64
	v_med3_f32 v85, v86, s26, v75
	v_med3_f32 v72, v72, s26, v75
	v_cvt_pk_fp8_f32 v88, v85, v72 op_sel:[0,0,1]
	v_add3_u32 v72, s33, v79, v77
	ds_write_b32 v72, v87
	v_add3_u32 v72, s33, v80, v82
	ds_write_b32 v72, v88
	v_mul_f32_e32 v72, 0x43800000, v53
	v_mul_f32_e32 v85, 0x43800000, v57
	v_med3_f32 v72, v72, s26, v75
	v_med3_f32 v85, v85, s26, v75
	v_cvt_pk_fp8_f32 v87, v72, v85
	v_mul_f32_e32 v86, 0x43800000, v61
	v_mul_f32_e32 v72, 0x43800000, v65
	v_med3_f32 v85, v86, s26, v75
	v_med3_f32 v72, v72, s26, v75
	v_cvt_pk_fp8_f32 v87, v85, v72 op_sel:[0,0,1]
	s_add_i32 s1, s17, s1
	v_add3_u32 v72, s33, v78, v83
	s_cmp_ge_i32 s1, s25
	ds_write_b32 v72, v87
	s_cbranch_scc1 .LBB0_212
	s_ashr_i32 s34, s1, 31
	s_lshr_b32 s34, s34, 23
	s_add_i32 s35, s1, s34
	s_ashr_i32 s34, s35, 9
	s_and_b32 s35, s35, 0xfe00
	s_sub_i32 s1, s1, s35
	s_ashr_i32 s35, s34, 31
	s_lshl_b64 s[34:35], s[34:35], 24
	v_lshl_add_u64 v[50:51], v[66:67], 0, s[34:35]
	s_sext_i32_i16 s34, s1
	s_bfe_u32 s34, s34, 0x4001b
	s_add_i32 s34, s1, s34
	s_sext_i32_i16 s35, s34
	s_and_b32 s34, s34, 0xfff0
	s_sub_i32 s1, s1, s34
	s_lshl_b32 s34, s35, 2
	s_sext_i32_i16 s1, s1
	s_andn2_b32 s34, s34, 63
	v_lshl_add_u32 v58, s1, 7, v69
	s_ashr_i32 s35, s34, 31
	v_lshl_add_u64 v[50:51], s[34:35], 2, v[50:51]
	v_lshlrev_b32_e32 v72, 2, v68
	v_ashrrev_i32_e32 v59, 31, v58
	v_lshl_add_u64 v[60:61], v[50:51], 0, v[72:73]
	v_lshlrev_b64 v[50:51], 13, v[58:59]
	v_lshl_add_u64 v[62:63], v[60:61], 0, v[50:51]
	v_or_b32_e32 v50, 1, v58
	v_ashrrev_i32_e32 v51, 31, v50
	v_lshlrev_b64 v[50:51], 13, v[50:51]
	v_lshl_add_u64 v[64:65], v[60:61], 0, v[50:51]
	global_load_dwordx4 v[50:53], v[62:63], off sc1 nt
	global_load_dwordx4 v[54:57], v[64:65], off sc1 nt
	v_or_b32_e32 v62, 2, v58
	v_ashrrev_i32_e32 v63, 31, v62
	v_or_b32_e32 v58, 3, v58
	v_lshlrev_b64 v[62:63], 13, v[62:63]
	v_ashrrev_i32_e32 v59, 31, v58
	v_lshl_add_u64 v[86:87], v[60:61], 0, v[62:63]
	v_lshlrev_b64 v[58:59], 13, v[58:59]
	v_lshl_add_u64 v[88:89], v[60:61], 0, v[58:59]
	global_load_dwordx4 v[58:61], v[86:87], off sc1 nt
	global_load_dwordx4 v[62:65], v[88:89], off sc1 nt
	s_branch .LBB0_212

; #define LAS __attribute__((address_space(3)))
; #define TB_LOAD(R_, t_) do { const int _t = (t_); if (_t < tot) { const int _b = _t / per, _r = _t % per; ttb_load(R_, src + (size_t)_b * K_ * N_, N_, (_r % kt) * 128, (_r / kt) * 64, C.tid); } } while (0)
; __device__ __forceinline__ void ttb_load(TReg& R, const float* src, int ld, int k0, int n0, int tid) {
;     const int kr = tid >> 4, nq = tid & 15;
; #pragma unroll
;     for (int rep = 0; rep < 4; ++rep) R.v[rep] = __builtin_nontemporal_load((const f32x4*)(src + (size_t)(k0 + 4 * kr + rep) * ld + n0 + 4 * nq)); }
; __device__ __forceinline__ void ttb_put(const TReg& R, LAS unsigned* tile, int tid) {
;     const int kr = tid >> 4, nq = tid & 15;
; #pragma unroll
;     for (int c = 0; c < 4; ++c) { const int n = 4 * nq + c;
;         tile[n * 32 + (kr ^ (n & 31))] = pk4_fp8(R.v[0][c] * W_FP8_SCALE, R.v[1][c] * W_FP8_SCALE, R.v[2][c] * W_FP8_SCALE, R.v[3][c] * W_FP8_SCALE); } }
; __device__ __forceinline__ void ttb_finish(LAS const unsigned* tile, unsigned char* dst, int ldd, int k0, int n0, int map, int tid) {
;     const int n = tid >> 3, kq = tid & 7, m = n & 31, ns = n0 + n; int r = ns;
;     if (map == 2) { const int j = ns >> 1, par = ns & 1; r = 256 * (j >> 7) + 128 * par + (j & 127); }
;     const u32x4 g = *(LAS const u32x4*)(tile + n * 32 + 4 * (kq ^ (m >> 2)));
;     const unsigned a0 = (m & 1) ? g.y : g.x, a1 = (m & 1) ? g.x : g.y, a2 = (m & 1) ? g.w : g.z, a3 = (m & 1) ? g.z : g.w;
;     u32x4 w; w.x = (m & 2) ? a2 : a0; w.y = (m & 2) ? a3 : a1; w.z = (m & 2) ? a0 : a2; w.w = (m & 2) ? a1 : a3;
;     __builtin_nontemporal_store(w, (u32x4*)(dst + (size_t)r * ldd + k0 + 16 * kq));
; }
; template <int K_, int N_, int MAP_> __device__ __forceinline__ void tjob_b(const Ctx& C, int bid, int G, const float* src, unsigned char* dstb, int nbatch) {
;     constexpr int kt = K_ / 128, ntile = N_ / 64, per = kt * ntile; const int tot = per * nbatch;
;     TReg R0, R1, R2, R3; int kbuf = 0;
;     ...
;     TB_LOAD(R0, bid); TB_LOAD(R1, bid + G); TB_LOAD(R2, bid + 2 * G); TB_LOAD(R3, bid + 3 * G);
; __global__ void __launch_bounds__(512, 2) mk_fwd(Args args) {
;     ...
;         fresh_tid(C); if (nconv) tjob_b<2048, 2048, 0>(C, C.bid, Gg, C.ka->in[I_WE2] + (size_t)(NEXP - E2_TAIL) * FF * D_, C.ws + WS_W2T + (size_t)(NEXP - E2_TAIL) * FF * D_, E2_TAIL);
.LBB0_269:
	v_mov_b32_e32 v70, v0
	s_andn2_b64 vcc, exec, s[20:21]
	s_mov_b64 s[0:1], s[70:71]
	s_cbranch_vccnz .LBB0_278
	v_mov_b64_e32 v[2:3], s[0:1]
	flat_load_dwordx2 v[2:3], v[2:3] offset:200
	v_readlane_b32 s10, v254, 0
	s_mov_b64 s[70:71], s[0:1]
	s_cmpk_lt_i32 s10, 0x1600
	s_mov_b64 s[0:1], 0x15000000
	v_ashrrev_i32_e32 v72, 2, v70
	s_cselect_b64 s[2:3], -1, 0
	s_cmpk_gt_i32 s10, 0x15ff
	v_lshlrev_b32_e32 v1, 4, v70
	v_readlane_b32 s11, v254, 1
	s_waitcnt vmcnt(0) lgkmcnt(0)
	v_lshl_add_u64 v[66:67], v[2:3], 0, s[0:1]
	s_cbranch_scc1 .LBB0_272
	s_ashr_i32 s0, s10, 31
	s_lshr_b32 s0, s0, 23
	s_add_i32 s1, s10, s0
	s_ashr_i32 s0, s1, 9
	s_and_b32 s1, s1, 0xfe00
	s_sub_i32 s6, s10, s1
	s_sext_i32_i16 s7, s6
	s_bfe_u32 s7, s7, 0x4001b
	s_add_i32 s7, s6, s7
	s_sext_i32_i16 s8, s7
	s_and_b32 s7, s7, 0xfff0
	s_sub_i32 s6, s6, s7
	s_ashr_i32 s1, s0, 31
	s_sext_i32_i16 s9, s6
	s_lshl_b32 s6, s8, 2
	s_lshl_b64 s[0:1], s[0:1], 24
	s_andn2_b32 s6, s6, 63
	v_and_b32_e32 v4, -4, v72
	s_ashr_i32 s7, s6, 31
	v_lshl_add_u64 v[2:3], v[66:67], 0, s[0:1]
	v_lshl_add_u32 v10, s9, 7, v4
	v_lshl_add_u64 v[2:3], s[6:7], 2, v[2:3]
	v_and_b32_e32 v4, 0xf0, v1
	v_mov_b32_e32 v5, 0
	v_ashrrev_i32_e32 v11, 31, v10
	v_lshl_add_u64 v[12:13], v[2:3], 0, v[4:5]
	v_lshlrev_b64 v[2:3], 13, v[10:11]
	v_lshl_add_u64 v[14:15], v[12:13], 0, v[2:3]
	v_or_b32_e32 v2, 1, v10
	v_ashrrev_i32_e32 v3, 31, v2
	v_lshlrev_b64 v[2:3], 13, v[2:3]
	v_lshl_add_u64 v[16:17], v[12:13], 0, v[2:3]
	global_load_dwordx4 v[2:5], v[14:15], off sc1 nt
	global_load_dwordx4 v[6:9], v[16:17], off sc1 nt
	v_or_b32_e32 v14, 2, v10
	v_ashrrev_i32_e32 v15, 31, v14
	v_or_b32_e32 v10, 3, v10
	v_lshlrev_b64 v[14:15], 13, v[14:15]
	v_ashrrev_i32_e32 v11, 31, v10
	v_lshl_add_u64 v[18:19], v[12:13], 0, v[14:15]
	v_lshlrev_b64 v[10:11], 13, v[10:11]
	v_lshl_add_u64 v[20:21], v[12:13], 0, v[10:11]
	global_load_dwordx4 v[10:13], v[18:19], off sc1 nt
	global_load_dwordx4 v[14:17], v[20:21], off sc1 nt
.LBB0_272:
	s_add_i32 s0, s28, s10
	s_cmpk_gt_i32 s0, 0x15ff
	s_cbranch_scc1 .LBB0_274
	s_ashr_i32 s1, s0, 31
	s_lshr_b32 s1, s1, 23
	s_add_i32 s1, s0, s1
	s_ashr_i32 s6, s1, 9
	s_and_b32 s1, s1, 0xfe00
	s_sub_i32 s1, s0, s1
	s_sext_i32_i16 s8, s1
	s_bfe_u32 s8, s8, 0x4001b
	s_add_i32 s8, s1, s8
	s_sext_i32_i16 s9, s8
	s_and_b32 s8, s8, 0xfff0
	s_ashr_i32 s7, s6, 31
	s_sub_i32 s1, s1, s8
	s_lshl_b32 s8, s9, 2
	s_lshl_b64 s[6:7], s[6:7], 24
	s_sext_i32_i16 s1, s1
	s_andn2_b32 s8, s8, 63
	v_and_b32_e32 v20, -4, v72
	s_ashr_i32 s9, s8, 31
	v_lshl_add_u64 v[18:19], v[66:67], 0, s[6:7]
	v_lshl_add_u32 v26, s1, 7, v20
	v_lshl_add_u64 v[18:19], s[8:9], 2, v[18:19]
	v_and_b32_e32 v20, 0xf0, v1
	v_mov_b32_e32 v21, 0
	v_ashrrev_i32_e32 v27, 31, v26
	v_lshl_add_u64 v[28:29], v[18:19], 0, v[20:21]
	v_lshlrev_b64 v[18:19], 13, v[26:27]
	v_lshl_add_u64 v[30:31], v[28:29], 0, v[18:19]
	v_or_b32_e32 v18, 1, v26
	v_ashrrev_i32_e32 v19, 31, v18
	v_lshlrev_b64 v[18:19], 13, v[18:19]
	v_lshl_add_u64 v[32:33], v[28:29], 0, v[18:19]
	global_load_dwordx4 v[18:21], v[30:31], off sc1 nt
	global_load_dwordx4 v[22:25], v[32:33], off sc1 nt
	v_or_b32_e32 v30, 2, v26
	v_ashrrev_i32_e32 v31, 31, v30
	v_or_b32_e32 v26, 3, v26
	v_lshlrev_b64 v[30:31], 13, v[30:31]
	v_ashrrev_i32_e32 v27, 31, v26
	v_lshl_add_u64 v[34:35], v[28:29], 0, v[30:31]
	v_lshlrev_b64 v[26:27], 13, v[26:27]
	v_lshl_add_u64 v[36:37], v[28:29], 0, v[26:27]
	global_load_dwordx4 v[26:29], v[34:35], off sc1 nt
	global_load_dwordx4 v[30:33], v[36:37], off sc1 nt
.LBB0_274:
	s_add_i32 s0, s0, s28
	s_cmpk_gt_i32 s0, 0x15ff
	s_cbranch_scc1 .LBB0_276
	s_ashr_i32 s1, s0, 31
	s_lshr_b32 s1, s1, 23
	s_add_i32 s1, s0, s1
	s_ashr_i32 s6, s1, 9
	s_and_b32 s1, s1, 0xfe00
	s_sub_i32 s1, s0, s1
	s_sext_i32_i16 s8, s1
	s_bfe_u32 s8, s8, 0x4001b
	s_add_i32 s8, s1, s8
	s_sext_i32_i16 s9, s8
	s_and_b32 s8, s8, 0xfff0
	s_ashr_i32 s7, s6, 31
	s_sub_i32 s1, s1, s8
	s_lshl_b32 s8, s9, 2
	s_lshl_b64 s[6:7], s[6:7], 24
	s_sext_i32_i16 s1, s1
	s_andn2_b32 s8, s8, 63
	v_and_b32_e32 v36, -4, v72
	s_ashr_i32 s9, s8, 31
	v_lshl_add_u64 v[34:35], v[66:67], 0, s[6:7]
	v_lshl_add_u32 v42, s1, 7, v36
	v_lshl_add_u64 v[34:35], s[8:9], 2, v[34:35]
	v_and_b32_e32 v36, 0xf0, v1
	v_mov_b32_e32 v37, 0
	v_ashrrev_i32_e32 v43, 31, v42
	v_lshl_add_u64 v[44:45], v[34:35], 0, v[36:37]
	v_lshlrev_b64 v[34:35], 13, v[42:43]
	v_lshl_add_u64 v[46:47], v[44:45], 0, v[34:35]
	v_or_b32_e32 v34, 1, v42
	v_ashrrev_i32_e32 v35, 31, v34
	v_lshlrev_b64 v[34:35], 13, v[34:35]
	v_lshl_add_u64 v[48:49], v[44:45], 0, v[34:35]
	global_load_dwordx4 v[34:37], v[46:47], off sc1 nt
	global_load_dwordx4 v[38:41], v[48:49], off sc1 nt
	v_or_b32_e32 v46, 2, v42
	v_ashrrev_i32_e32 v47, 31, v46
	v_or_b32_e32 v42, 3, v42
	v_lshlrev_b64 v[46:47], 13, v[46:47]
	v_ashrrev_i32_e32 v43, 31, v42
	v_lshl_add_u64 v[50:51], v[44:45], 0, v[46:47]
	v_lshlrev_b64 v[42:43], 13, v[42:43]
	v_lshl_add_u64 v[52:53], v[44:45], 0, v[42:43]
	global_load_dwordx4 v[42:45], v[50:51], off sc1 nt
	global_load_dwordx4 v[46:49], v[52:53], off sc1 nt
.LBB0_276:
	s_add_i32 s0, s0, s28
	s_cmpk_gt_i32 s0, 0x15ff
	s_cbranch_scc1 .LBB0_279
	s_ashr_i32 s1, s0, 31
	s_lshr_b32 s1, s1, 23
	s_add_i32 s1, s0, s1
	s_ashr_i32 s6, s1, 9
	s_and_b32 s1, s1, 0xfe00
	s_sub_i32 s8, s0, s1
	s_ashr_i32 s7, s6, 31
	s_lshl_b64 s[0:1], s[6:7], 24
	s_sext_i32_i16 s6, s8
	s_bfe_u32 s6, s6, 0x4001b
	s_add_i32 s6, s8, s6
	s_sext_i32_i16 s7, s6
	s_and_b32 s6, s6, 0xfff0
	s_sub_i32 s6, s8, s6
	s_sext_i32_i16 s8, s6
	s_lshl_b32 s6, s7, 2
	s_andn2_b32 s6, s6, 63
	v_and_b32_e32 v52, -4, v72
	s_ashr_i32 s7, s6, 31
	v_lshl_add_u64 v[50:51], v[66:67], 0, s[0:1]
	v_lshl_add_u32 v58, s8, 7, v52
	v_lshl_add_u64 v[50:51], s[6:7], 2, v[50:51]
	v_and_b32_e32 v52, 0xf0, v1
	v_mov_b32_e32 v53, 0
	v_ashrrev_i32_e32 v59, 31, v58
	v_lshl_add_u64 v[60:61], v[50:51], 0, v[52:53]
	v_lshlrev_b64 v[50:51], 13, v[58:59]
	v_lshl_add_u64 v[62:63], v[60:61], 0, v[50:51]
	v_or_b32_e32 v50, 1, v58
	v_ashrrev_i32_e32 v51, 31, v50
	v_lshlrev_b64 v[50:51], 13, v[50:51]
	v_lshl_add_u64 v[64:65], v[60:61], 0, v[50:51]
	global_load_dwordx4 v[50:53], v[62:63], off sc1 nt
	global_load_dwordx4 v[54:57], v[64:65], off sc1 nt
	v_or_b32_e32 v62, 2, v58
	v_ashrrev_i32_e32 v63, 31, v62
	v_or_b32_e32 v58, 3, v58
	v_lshlrev_b64 v[62:63], 13, v[62:63]
	v_ashrrev_i32_e32 v59, 31, v58
	v_lshl_add_u64 v[68:69], v[60:61], 0, v[62:63]
	v_lshlrev_b64 v[58:59], 13, v[58:59]
	v_lshl_add_u64 v[74:75], v[60:61], 0, v[58:59]
	global_load_dwordx4 v[58:61], v[68:69], off sc1 nt
	global_load_dwordx4 v[62:65], v[74:75], off sc1 nt
	s_andn2_b64 vcc, exec, s[2:3]
	s_cbranch_vccnz .LBB0_296
	s_branch .LBB0_280

; #define LAS __attribute__((address_space(3)))
; __device__ __forceinline__ void ttb_put(const TReg& R, LAS unsigned* tile, int tid) {
;     const int kr = tid >> 4, nq = tid & 15;
; #pragma unroll
;     for (int c = 0; c < 4; ++c) { const int n = 4 * nq + c;
;         tile[n * 32 + (kr ^ (n & 31))] = pk4_fp8(R.v[0][c] * W_FP8_SCALE, R.v[1][c] * W_FP8_SCALE, R.v[2][c] * W_FP8_SCALE, R.v[3][c] * W_FP8_SCALE); } }
.Lcv_jt_0:
	v_mul_f32_e32 v72, 0x43800000, v2
	v_mul_f32_e32 v85, 0x43800000, v6
	v_med3_f32 v72, v72, s17, v79
	v_med3_f32 v85, v85, s17, v79
	v_cvt_pk_fp8_f32 v87, v72, v85
	v_mul_f32_e32 v86, 0x43800000, v10
	v_mul_f32_e32 v72, 0x43800000, v14
	v_med3_f32 v85, v86, s17, v79
	v_med3_f32 v72, v72, s17, v79
	v_cvt_pk_fp8_f32 v87, v85, v72 op_sel:[0,0,1]
	v_mul_f32_e32 v72, 0x43800000, v3
	v_mul_f32_e32 v85, 0x43800000, v7
	v_med3_f32 v72, v72, s17, v79
	v_med3_f32 v85, v85, s17, v79
	v_cvt_pk_fp8_f32 v88, v72, v85
	v_mul_f32_e32 v86, 0x43800000, v11
	v_mul_f32_e32 v72, 0x43800000, v15
	v_med3_f32 v85, v86, s17, v79
	v_med3_f32 v72, v72, s17, v79
	s_lshl_b32 s2, s13, 13
	v_cvt_pk_fp8_f32 v88, v85, v72 op_sel:[0,0,1]
	s_add_i32 s20, s2, 0
	v_add3_u32 v72, s20, v1, v80
	ds_write_b32 v72, v87
	v_add3_u32 v72, s20, v69, v81
	ds_write_b32 v72, v88
	v_mul_f32_e32 v72, 0x43800000, v4
	v_mul_f32_e32 v85, 0x43800000, v8
	v_med3_f32 v72, v72, s17, v79
	v_med3_f32 v85, v85, s17, v79
	v_cvt_pk_fp8_f32 v87, v72, v85
	v_mul_f32_e32 v86, 0x43800000, v12
	v_mul_f32_e32 v72, 0x43800000, v16
	v_med3_f32 v85, v86, s17, v79
	v_med3_f32 v72, v72, s17, v79
	v_cvt_pk_fp8_f32 v87, v85, v72 op_sel:[0,0,1]
	v_mul_f32_e32 v72, 0x43800000, v5
	v_mul_f32_e32 v85, 0x43800000, v9
	v_med3_f32 v72, v72, s17, v79
	v_med3_f32 v85, v85, s17, v79
	v_cvt_pk_fp8_f32 v88, v72, v85
	v_mul_f32_e32 v86, 0x43800000, v13
	v_mul_f32_e32 v72, 0x43800000, v17
	v_med3_f32 v85, v86, s17, v79
	v_med3_f32 v72, v72, s17, v79
	v_cvt_pk_fp8_f32 v88, v85, v72 op_sel:[0,0,1]
	s_add_i32 s18, s19, s12
	s_cmpk_gt_i32 s18, 0x15ff
	v_add3_u32 v72, s20, v74, v82
	s_cselect_b64 s[2:3], -1, 0
	ds_write_b32 v72, v87
	v_add3_u32 v72, s20, v75, v83
	s_and_b64 vcc, exec, s[2:3]
	ds_write_b32 v72, v88
	s_cbranch_vccnz .LBB0_285
	s_ashr_i32 s21, s18, 31
	s_lshr_b32 s21, s21, 23
	s_add_i32 s21, s18, s21
	s_ashr_i32 s22, s21, 9
	s_and_b32 s21, s21, 0xfe00
	s_ashr_i32 s23, s22, 31
	s_sub_i32 s21, s18, s21
	s_lshl_b64 s[22:23], s[22:23], 24
	v_lshl_add_u64 v[2:3], v[66:67], 0, s[22:23]
	s_sext_i32_i16 s22, s21
	s_bfe_u32 s22, s22, 0x4001b
	s_add_i32 s22, s21, s22
	s_sext_i32_i16 s23, s22
	s_and_b32 s22, s22, 0xfff0
	s_sub_i32 s21, s21, s22
	s_lshl_b32 s22, s23, 2
	s_sext_i32_i16 s21, s21
	s_andn2_b32 s22, s22, 63
	v_lshl_add_u32 v10, s21, 7, v78
	s_ashr_i32 s23, s22, 31
	v_lshl_add_u64 v[2:3], s[22:23], 2, v[2:3]
	v_lshlrev_b32_e32 v72, 2, v68
	v_ashrrev_i32_e32 v11, 31, v10
	v_lshl_add_u64 v[12:13], v[2:3], 0, v[72:73]
	v_lshlrev_b64 v[2:3], 13, v[10:11]
	v_lshl_add_u64 v[14:15], v[12:13], 0, v[2:3]
	v_or_b32_e32 v2, 1, v10
	v_ashrrev_i32_e32 v3, 31, v2
	v_lshlrev_b64 v[2:3], 13, v[2:3]
	v_lshl_add_u64 v[16:17], v[12:13], 0, v[2:3]
	global_load_dwordx4 v[2:5], v[14:15], off sc1 nt
	global_load_dwordx4 v[6:9], v[16:17], off sc1 nt
	v_or_b32_e32 v14, 2, v10
	v_ashrrev_i32_e32 v15, 31, v14
	v_or_b32_e32 v10, 3, v10
	v_lshlrev_b64 v[14:15], 13, v[14:15]
	v_ashrrev_i32_e32 v11, 31, v10
	v_lshl_add_u64 v[86:87], v[12:13], 0, v[14:15]
	v_lshlrev_b64 v[10:11], 13, v[10:11]
	v_lshl_add_u64 v[88:89], v[12:13], 0, v[10:11]
	global_load_dwordx4 v[10:13], v[86:87], off sc1 nt
	global_load_dwordx4 v[14:17], v[88:89], off sc1 nt

; #define LAS __attribute__((address_space(3)))
; __device__ __forceinline__ void ttb_put(const TReg& R, LAS unsigned* tile, int tid) {
;     const int kr = tid >> 4, nq = tid & 15;
; #pragma unroll
;     for (int c = 0; c < 4; ++c) { const int n = 4 * nq + c;
;         tile[n * 32 + (kr ^ (n & 31))] = pk4_fp8(R.v[0][c] * W_FP8_SCALE, R.v[1][c] * W_FP8_SCALE, R.v[2][c] * W_FP8_SCALE, R.v[3][c] * W_FP8_SCALE); } }
.Lcv_jt_1:
	v_mul_f32_e32 v72, 0x43800000, v18
	v_mul_f32_e32 v85, 0x43800000, v22
	v_med3_f32 v72, v72, s17, v79
	v_med3_f32 v85, v85, s17, v79
	v_cvt_pk_fp8_f32 v87, v72, v85
	v_mul_f32_e32 v86, 0x43800000, v26
	v_mul_f32_e32 v72, 0x43800000, v30
	v_med3_f32 v85, v86, s17, v79
	v_med3_f32 v72, v72, s17, v79
	v_cvt_pk_fp8_f32 v87, v85, v72 op_sel:[0,0,1]
	s_lshl_b32 s21, s21, 13
	s_add_i32 s21, s21, 0
	v_add3_u32 v72, s21, v1, v80
	ds_write_b32 v72, v87
	v_mul_f32_e32 v72, 0x43800000, v19
	v_mul_f32_e32 v85, 0x43800000, v23
	v_med3_f32 v72, v72, s17, v79
	v_med3_f32 v85, v85, s17, v79
	v_cvt_pk_fp8_f32 v87, v72, v85
	v_mul_f32_e32 v86, 0x43800000, v27
	v_mul_f32_e32 v72, 0x43800000, v31
	v_med3_f32 v85, v86, s17, v79
	v_med3_f32 v72, v72, s17, v79
	v_cvt_pk_fp8_f32 v87, v85, v72 op_sel:[0,0,1]
	v_mul_f32_e32 v72, 0x43800000, v20
	v_mul_f32_e32 v85, 0x43800000, v24
	v_med3_f32 v72, v72, s17, v79
	v_med3_f32 v85, v85, s17, v79
	v_cvt_pk_fp8_f32 v88, v72, v85
	v_mul_f32_e32 v86, 0x43800000, v28
	v_mul_f32_e32 v72, 0x43800000, v32
	v_med3_f32 v85, v86, s17, v79
	v_med3_f32 v72, v72, s17, v79
	v_cvt_pk_fp8_f32 v88, v85, v72 op_sel:[0,0,1]
	v_add3_u32 v72, s21, v69, v81
	ds_write_b32 v72, v87
	v_add3_u32 v72, s21, v74, v82
	ds_write_b32 v72, v88
	v_mul_f32_e32 v72, 0x43800000, v21
	v_mul_f32_e32 v85, 0x43800000, v25
	v_med3_f32 v72, v72, s17, v79
	v_med3_f32 v85, v85, s17, v79
	v_cvt_pk_fp8_f32 v87, v72, v85
	v_mul_f32_e32 v86, 0x43800000, v29
	v_mul_f32_e32 v72, 0x43800000, v33
	v_med3_f32 v85, v86, s17, v79
	v_med3_f32 v72, v72, s17, v79
	v_cvt_pk_fp8_f32 v87, v85, v72 op_sel:[0,0,1]
	s_add_i32 s22, s16, s19
	v_add3_u32 v72, s21, v75, v83
	s_cmpk_gt_i32 s22, 0x15ff
	ds_write_b32 v72, v87
	s_cbranch_scc1 .LBB0_288
	s_ashr_i32 s23, s22, 31
	s_lshr_b32 s23, s23, 23
	s_add_i32 s23, s22, s23
	s_ashr_i32 s24, s23, 9
	s_and_b32 s23, s23, 0xfe00
	s_ashr_i32 s25, s24, 31
	s_sub_i32 s26, s22, s23
	s_lshl_b64 s[22:23], s[24:25], 24
	v_lshl_add_u64 v[18:19], v[66:67], 0, s[22:23]
	s_sext_i32_i16 s22, s26
	s_bfe_u32 s22, s22, 0x4001b
	s_add_i32 s22, s26, s22
	s_sext_i32_i16 s23, s22
	s_and_b32 s22, s22, 0xfff0
	s_sub_i32 s22, s26, s22
	s_sext_i32_i16 s24, s22
	s_lshl_b32 s22, s23, 2
	s_andn2_b32 s22, s22, 63
	v_lshl_add_u32 v26, s24, 7, v78
	s_ashr_i32 s23, s22, 31
	v_lshl_add_u64 v[18:19], s[22:23], 2, v[18:19]
	v_lshlrev_b32_e32 v72, 2, v68
	v_ashrrev_i32_e32 v27, 31, v26
	v_lshl_add_u64 v[28:29], v[18:19], 0, v[72:73]
	v_lshlrev_b64 v[18:19], 13, v[26:27]
	v_lshl_add_u64 v[30:31], v[28:29], 0, v[18:19]
	v_or_b32_e32 v18, 1, v26
	v_ashrrev_i32_e32 v19, 31, v18
	v_lshlrev_b64 v[18:19], 13, v[18:19]
	v_lshl_add_u64 v[32:33], v[28:29], 0, v[18:19]
	global_load_dwordx4 v[18:21], v[30:31], off sc1 nt
	global_load_dwordx4 v[22:25], v[32:33], off sc1 nt
	v_or_b32_e32 v30, 2, v26
	v_ashrrev_i32_e32 v31, 31, v30
	v_or_b32_e32 v26, 3, v26
	v_lshlrev_b64 v[30:31], 13, v[30:31]
	v_ashrrev_i32_e32 v27, 31, v26
	v_lshl_add_u64 v[86:87], v[28:29], 0, v[30:31]
	v_lshlrev_b64 v[26:27], 13, v[26:27]
	v_lshl_add_u64 v[88:89], v[28:29], 0, v[26:27]
	global_load_dwordx4 v[26:29], v[86:87], off sc1 nt
	global_load_dwordx4 v[30:33], v[88:89], off sc1 nt

; #define LAS __attribute__((address_space(3)))
; __device__ __forceinline__ void ttb_put(const TReg& R, LAS unsigned* tile, int tid) {
;     const int kr = tid >> 4, nq = tid & 15;
; #pragma unroll
;     for (int c = 0; c < 4; ++c) { const int n = 4 * nq + c;
;         tile[n * 32 + (kr ^ (n & 31))] = pk4_fp8(R.v[0][c] * W_FP8_SCALE, R.v[1][c] * W_FP8_SCALE, R.v[2][c] * W_FP8_SCALE, R.v[3][c] * W_FP8_SCALE); } }
.Lcv_jt_2:
	v_mul_f32_e32 v72, 0x43800000, v34
	v_mul_f32_e32 v85, 0x43800000, v38
	v_med3_f32 v72, v72, s17, v79
	v_med3_f32 v85, v85, s17, v79
	v_cvt_pk_fp8_f32 v87, v72, v85
	v_mul_f32_e32 v86, 0x43800000, v42
	v_mul_f32_e32 v72, 0x43800000, v46
	v_med3_f32 v85, v86, s17, v79
	v_med3_f32 v72, v72, s17, v79
	v_cvt_pk_fp8_f32 v87, v85, v72 op_sel:[0,0,1]
	s_lshl_b32 s21, s13, 13
	s_add_i32 s21, s21, 0
	v_add3_u32 v72, s21, v1, v80
	ds_write_b32 v72, v87
	v_mul_f32_e32 v72, 0x43800000, v35
	v_mul_f32_e32 v85, 0x43800000, v39
	v_med3_f32 v72, v72, s17, v79
	v_med3_f32 v85, v85, s17, v79
	v_cvt_pk_fp8_f32 v87, v72, v85
	v_mul_f32_e32 v86, 0x43800000, v43
	v_mul_f32_e32 v72, 0x43800000, v47
	v_med3_f32 v85, v86, s17, v79
	v_med3_f32 v72, v72, s17, v79
	v_cvt_pk_fp8_f32 v87, v85, v72 op_sel:[0,0,1]
	v_mul_f32_e32 v72, 0x43800000, v36
	v_mul_f32_e32 v85, 0x43800000, v40
	v_med3_f32 v72, v72, s17, v79
	v_med3_f32 v85, v85, s17, v79
	v_cvt_pk_fp8_f32 v88, v72, v85
	v_mul_f32_e32 v86, 0x43800000, v44
	v_mul_f32_e32 v72, 0x43800000, v48
	v_med3_f32 v85, v86, s17, v79
	v_med3_f32 v72, v72, s17, v79
	v_cvt_pk_fp8_f32 v88, v85, v72 op_sel:[0,0,1]
	v_add3_u32 v72, s21, v69, v81
	ds_write_b32 v72, v87
	v_add3_u32 v72, s21, v74, v82
	ds_write_b32 v72, v88
	v_mul_f32_e32 v72, 0x43800000, v37
	v_mul_f32_e32 v85, 0x43800000, v41
	v_med3_f32 v72, v72, s17, v79
	v_med3_f32 v85, v85, s17, v79
	v_cvt_pk_fp8_f32 v87, v72, v85
	v_mul_f32_e32 v86, 0x43800000, v45
	v_mul_f32_e32 v72, 0x43800000, v49
	v_med3_f32 v85, v86, s17, v79
	v_med3_f32 v72, v72, s17, v79
	v_cvt_pk_fp8_f32 v87, v85, v72 op_sel:[0,0,1]
	s_add_i32 s22, s15, s19
	v_add3_u32 v72, s21, v75, v83
	s_cmpk_gt_i32 s22, 0x15ff
	ds_write_b32 v72, v87
	s_cbranch_scc1 .LBB0_292
	s_ashr_i32 s23, s22, 31
	s_lshr_b32 s23, s23, 23
	s_add_i32 s23, s22, s23
	s_ashr_i32 s24, s23, 9
	s_and_b32 s23, s23, 0xfe00
	s_ashr_i32 s25, s24, 31
	s_sub_i32 s26, s22, s23
	s_lshl_b64 s[22:23], s[24:25], 24
	v_lshl_add_u64 v[34:35], v[66:67], 0, s[22:23]
	s_sext_i32_i16 s22, s26
	s_bfe_u32 s22, s22, 0x4001b
	s_add_i32 s22, s26, s22
	s_sext_i32_i16 s23, s22
	s_and_b32 s22, s22, 0xfff0
	s_sub_i32 s22, s26, s22
	s_sext_i32_i16 s24, s22
	s_lshl_b32 s22, s23, 2
	s_andn2_b32 s22, s22, 63
	v_lshl_add_u32 v42, s24, 7, v78
	s_ashr_i32 s23, s22, 31
	v_lshl_add_u64 v[34:35], s[22:23], 2, v[34:35]
	v_lshlrev_b32_e32 v72, 2, v68
	v_ashrrev_i32_e32 v43, 31, v42
	v_lshl_add_u64 v[44:45], v[34:35], 0, v[72:73]
	v_lshlrev_b64 v[34:35], 13, v[42:43]
	v_lshl_add_u64 v[46:47], v[44:45], 0, v[34:35]
	v_or_b32_e32 v34, 1, v42
	v_ashrrev_i32_e32 v35, 31, v34
	v_lshlrev_b64 v[34:35], 13, v[34:35]
	v_lshl_add_u64 v[48:49], v[44:45], 0, v[34:35]
	global_load_dwordx4 v[34:37], v[46:47], off sc1 nt
	global_load_dwordx4 v[38:41], v[48:49], off sc1 nt
	v_or_b32_e32 v46, 2, v42
	v_ashrrev_i32_e32 v47, 31, v46
	v_or_b32_e32 v42, 3, v42
	v_lshlrev_b64 v[46:47], 13, v[46:47]
	v_ashrrev_i32_e32 v43, 31, v42
	v_lshl_add_u64 v[86:87], v[44:45], 0, v[46:47]
	v_lshlrev_b64 v[42:43], 13, v[42:43]
	v_lshl_add_u64 v[88:89], v[44:45], 0, v[42:43]
	global_load_dwordx4 v[42:45], v[86:87], off sc1 nt
	global_load_dwordx4 v[46:49], v[88:89], off sc1 nt

; #define LAS __attribute__((address_space(3)))
; __device__ __forceinline__ void ttb_put(const TReg& R, LAS unsigned* tile, int tid) {
;     const int kr = tid >> 4, nq = tid & 15;
; #pragma unroll
;     for (int c = 0; c < 4; ++c) { const int n = 4 * nq + c;
;         tile[n * 32 + (kr ^ (n & 31))] = pk4_fp8(R.v[0][c] * W_FP8_SCALE, R.v[1][c] * W_FP8_SCALE, R.v[2][c] * W_FP8_SCALE, R.v[3][c] * W_FP8_SCALE); } }
.Lcv_jt_3:
	v_mul_f32_e32 v72, 0x43800000, v50
	v_mul_f32_e32 v85, 0x43800000, v54
	v_med3_f32 v72, v72, s17, v79
	v_med3_f32 v85, v85, s17, v79
	v_cvt_pk_fp8_f32 v87, v72, v85
	v_mul_f32_e32 v86, 0x43800000, v58
	v_mul_f32_e32 v72, 0x43800000, v62
	v_med3_f32 v85, v86, s17, v79
	v_med3_f32 v72, v72, s17, v79
	v_cvt_pk_fp8_f32 v87, v85, v72 op_sel:[0,0,1]
	s_lshl_b32 s21, s13, 13
	s_add_i32 s21, s21, 0
	v_add3_u32 v72, s21, v1, v80
	ds_write_b32 v72, v87
	v_mul_f32_e32 v72, 0x43800000, v51
	v_mul_f32_e32 v85, 0x43800000, v55
	v_med3_f32 v72, v72, s17, v79
	v_med3_f32 v85, v85, s17, v79
	v_cvt_pk_fp8_f32 v87, v72, v85
	v_mul_f32_e32 v86, 0x43800000, v59
	v_mul_f32_e32 v72, 0x43800000, v63
	v_med3_f32 v85, v86, s17, v79
	v_med3_f32 v72, v72, s17, v79
	v_cvt_pk_fp8_f32 v87, v85, v72 op_sel:[0,0,1]
	v_mul_f32_e32 v72, 0x43800000, v52
	v_mul_f32_e32 v85, 0x43800000, v56
	v_med3_f32 v72, v72, s17, v79
	v_med3_f32 v85, v85, s17, v79
	v_cvt_pk_fp8_f32 v88, v72, v85
	v_mul_f32_e32 v86, 0x43800000, v60
	v_mul_f32_e32 v72, 0x43800000, v64
	v_med3_f32 v85, v86, s17, v79
	v_med3_f32 v72, v72, s17, v79
	v_cvt_pk_fp8_f32 v88, v85, v72 op_sel:[0,0,1]
	v_add3_u32 v72, s21, v69, v81
	ds_write_b32 v72, v87
	v_add3_u32 v72, s21, v74, v82
	ds_write_b32 v72, v88
	v_mul_f32_e32 v72, 0x43800000, v53
	v_mul_f32_e32 v85, 0x43800000, v57
	v_med3_f32 v72, v72, s17, v79
	v_med3_f32 v85, v85, s17, v79
	v_cvt_pk_fp8_f32 v87, v72, v85
	v_mul_f32_e32 v86, 0x43800000, v61
	v_mul_f32_e32 v72, 0x43800000, v65
	v_med3_f32 v85, v86, s17, v79
	v_med3_f32 v72, v72, s17, v79
	v_cvt_pk_fp8_f32 v87, v85, v72 op_sel:[0,0,1]
	s_add_i32 s19, s14, s19
	v_add3_u32 v72, s21, v75, v83
	s_cmpk_gt_i32 s19, 0x15ff
	ds_write_b32 v72, v87
	s_cbranch_scc1 .LBB0_281
	s_ashr_i32 s22, s19, 31
	s_lshr_b32 s22, s22, 23
	s_add_i32 s23, s19, s22
	s_ashr_i32 s22, s23, 9
	s_and_b32 s23, s23, 0xfe00
	s_sub_i32 s19, s19, s23
	s_ashr_i32 s23, s22, 31
	s_lshl_b64 s[22:23], s[22:23], 24
	v_lshl_add_u64 v[50:51], v[66:67], 0, s[22:23]
	s_sext_i32_i16 s22, s19
	s_bfe_u32 s22, s22, 0x4001b
	s_add_i32 s22, s19, s22
	s_sext_i32_i16 s23, s22
	s_and_b32 s22, s22, 0xfff0
	s_sub_i32 s19, s19, s22
	s_lshl_b32 s22, s23, 2
	s_sext_i32_i16 s19, s19
	s_andn2_b32 s22, s22, 63
	v_lshl_add_u32 v58, s19, 7, v78
	s_ashr_i32 s23, s22, 31
	v_lshl_add_u64 v[50:51], s[22:23], 2, v[50:51]
	v_lshlrev_b32_e32 v72, 2, v68
	v_ashrrev_i32_e32 v59, 31, v58
	v_lshl_add_u64 v[60:61], v[50:51], 0, v[72:73]
	v_lshlrev_b64 v[50:51], 13, v[58:59]
	v_lshl_add_u64 v[62:63], v[60:61], 0, v[50:51]
	v_or_b32_e32 v50, 1, v58
	v_ashrrev_i32_e32 v51, 31, v50
	v_lshlrev_b64 v[50:51], 13, v[50:51]
	v_lshl_add_u64 v[64:65], v[60:61], 0, v[50:51]
	global_load_dwordx4 v[50:53], v[62:63], off sc1 nt
	global_load_dwordx4 v[54:57], v[64:65], off sc1 nt
	v_or_b32_e32 v62, 2, v58
	v_ashrrev_i32_e32 v63, 31, v62
	v_or_b32_e32 v58, 3, v58
	v_lshlrev_b64 v[62:63], 13, v[62:63]
	v_ashrrev_i32_e32 v59, 31, v58
	v_lshl_add_u64 v[86:87], v[60:61], 0, v[62:63]
	v_lshlrev_b64 v[58:59], 13, v[58:59]
	v_lshl_add_u64 v[88:89], v[60:61], 0, v[58:59]
	global_load_dwordx4 v[58:61], v[86:87], off sc1 nt
	global_load_dwordx4 v[62:65], v[88:89], off sc1 nt
	s_branch .LBB0_281
